# pads removed + topk key-row loads of a half issued up front (tag constants rematerialized to free the VGPRs)
# speedup vs baseline: 1.0172x; 1.0100x over previous
.LBB0_704:
	v_cndmask_b32_e64 v0, 0, 1, s[6:7]
	s_lshl_b32 s36, s8, 8
	v_cmp_ne_u32_e32 vcc, 1, v0
	v_lshl_add_u64 v[0:1], v[178:179], 0, s[36:37]
	global_load_dwordx4 v[44:47], v[0:1], off
	global_load_dwordx4 v[40:43], v[0:1], off offset:32
	global_load_dwordx4 v[36:39], v[0:1], off offset:64
	global_load_dwordx4 v[32:35], v[0:1], off offset:96
	global_load_dwordx4 v[28:31], v[0:1], off offset:128
	global_load_dwordx4 v[24:27], v[0:1], off offset:160
	global_load_dwordx4 v[20:23], v[0:1], off offset:192
	global_load_dwordx4 v[16:19], v[0:1], off offset:224
	v_lshl_or_b32 v180, s8, 7, v209
	v_ashrrev_i32_e32 v181, 31, v180
	v_lshlrev_b64 v[0:1], 8, v[180:181]
	v_lshl_add_u64 v[60:61], v[64:65], 0, v[0:1]
	global_load_dwordx4 v[0:3], v[60:61], off
	global_load_dwordx4 v[48:51], v[60:61], off offset:32
	global_load_dwordx4 v[52:55], v[60:61], off offset:64
	global_load_dwordx4 v[56:59], v[60:61], off offset:96
	global_load_dwordx4 v[68:71], v[60:61], off offset:128
	global_load_dwordx4 v[72:75], v[60:61], off offset:160
	global_load_dwordx4 v[76:79], v[60:61], off offset:192
	global_load_dwordx4 v[80:83], v[60:61], off offset:224
	s_mov_b32 s12, 0x2000
	s_mov_b32 s13, 0
	v_lshl_add_u64 v[186:187], v[60:61], 0, s[12:13]
	global_load_dwordx4 v[84:87], v[186:187], off
	global_load_dwordx4 v[88:91], v[186:187], off offset:32
	global_load_dwordx4 v[92:95], v[186:187], off offset:64
	global_load_dwordx4 v[96:99], v[186:187], off offset:96
	global_load_dwordx4 v[100:103], v[186:187], off offset:128
	global_load_dwordx4 v[104:107], v[186:187], off offset:160
	global_load_dwordx4 v[108:111], v[186:187], off offset:192
	global_load_dwordx4 v[112:115], v[186:187], off offset:224
	v_lshl_add_u64 v[188:189], v[186:187], 0, s[12:13]
	global_load_dwordx4 v[116:119], v[188:189], off
	global_load_dwordx4 v[120:123], v[188:189], off offset:32
	global_load_dwordx4 v[124:127], v[188:189], off offset:64
	global_load_dwordx4 v[128:131], v[188:189], off offset:96
	global_load_dwordx4 v[132:135], v[188:189], off offset:128
	global_load_dwordx4 v[136:139], v[188:189], off offset:160
	global_load_dwordx4 v[140:143], v[188:189], off offset:192
	global_load_dwordx4 v[152:155], v[188:189], off offset:224
	v_lshl_add_u64 v[186:187], v[188:189], 0, s[12:13]
	global_load_dwordx4 v[156:159], v[186:187], off
	global_load_dwordx4 v[160:163], v[186:187], off offset:32
	global_load_dwordx4 v[164:167], v[186:187], off offset:64
	global_load_dwordx4 v[168:171], v[186:187], off offset:96
	s_waitcnt vmcnt(24)
	v_mfma_f32_32x32x16_bf16 v[0:15], v[0:3], v[44:47], 0
	v_mfma_f32_32x32x16_bf16 v[0:15], v[48:51], v[40:43], v[0:15]
	v_mfma_f32_32x32x16_bf16 v[0:15], v[52:55], v[36:39], v[0:15]
	v_mfma_f32_32x32x16_bf16 v[0:15], v[56:59], v[32:35], v[0:15]
	global_load_dwordx4 v[48:51], v[186:187], off offset:128
	global_load_dwordx4 v[52:55], v[186:187], off offset:160
	global_load_dwordx4 v[56:59], v[186:187], off offset:192
	global_load_dwordx4 v[60:63], v[186:187], off offset:224
	s_waitcnt vmcnt(27)
	v_mfma_f32_32x32x16_bf16 v[0:15], v[68:71], v[28:31], v[0:15]
	s_waitcnt vmcnt(26)
	v_mfma_f32_32x32x16_bf16 v[0:15], v[72:75], v[24:27], v[0:15]
	s_waitcnt vmcnt(25)
	v_mfma_f32_32x32x16_bf16 v[0:15], v[76:79], v[20:23], v[0:15]
	s_waitcnt vmcnt(24)
	v_mfma_f32_32x32x16_bf16 v[0:15], v[80:83], v[16:19], v[0:15]
	v_or_b32_e32 v172, 1, v66
	v_xor_b32_e32 v174, 0x7e, v66
	s_nop 9
	v_cmp_gt_i32_e64 s[6:7], 0, v1
	v_xor_b32_e32 v67, 0x7f, v66
	v_and_b32_e32 v1, 0xffffff80, v1
	v_cndmask_b32_e64 v172, v174, v172, s[6:7]
	v_cmp_gt_i32_e64 s[6:7], 0, v0
	v_and_b32_e32 v0, 0xffffff80, v0
	v_or_b32_e32 v210, v172, v1
	v_cndmask_b32_e64 v67, v67, v66, s[6:7]
	v_or_b32_e32 v211, v67, v0
	v_or_b32_e32 v1, 3, v66
	v_xor_b32_e32 v173, 0x7c, v66
	v_cmp_gt_i32_e64 s[6:7], 0, v3
	v_or_b32_e32 v0, 2, v66
	v_xor_b32_e32 v190, 0x7d, v66
	v_cndmask_b32_e64 v1, v173, v1, s[6:7]
	v_cmp_gt_i32_e64 s[6:7], 0, v2
	v_and_b32_e32 v3, 0xffffff80, v3
	v_and_b32_e32 v2, 0xffffff80, v2
	v_cndmask_b32_e64 v0, v190, v0, s[6:7]
	v_or_b32_e32 v173, v1, v3
	v_or_b32_e32 v1, 9, v66
	v_xor_b32_e32 v3, 0x76, v66
	v_cmp_gt_i32_e64 s[6:7], 0, v5
	v_or_b32_e32 v212, v0, v2
	v_or_b32_e32 v0, 8, v66
	v_cndmask_b32_e64 v1, v3, v1, s[6:7]
	v_xor_b32_e32 v2, 0x77, v66
	v_cmp_gt_i32_e64 s[6:7], 0, v4
	v_and_b32_e32 v3, 0xffffff80, v4
	s_nop 0
	v_cndmask_b32_e64 v0, v2, v0, s[6:7]
	v_and_b32_e32 v2, 0xffffff80, v5
	v_or_b32_e32 v213, v1, v2
	v_or_b32_e32 v214, v0, v3
	v_or_b32_e32 v1, 11, v66
	v_xor_b32_e32 v3, 0x74, v66
	v_cmp_gt_i32_e64 s[6:7], 0, v7
	v_or_b32_e32 v0, 10, v66
	v_xor_b32_e32 v2, 0x75, v66
	v_cndmask_b32_e64 v1, v3, v1, s[6:7]
	v_cmp_gt_i32_e64 s[6:7], 0, v6
	v_and_b32_e32 v3, 0xffffff80, v6
	s_nop 0
	v_cndmask_b32_e64 v0, v2, v0, s[6:7]
	v_and_b32_e32 v2, 0xffffff80, v7
	v_or_b32_e32 v215, v1, v2
	v_or_b32_e32 v216, v0, v3
	v_or_b32_e32 v1, 17, v66
	v_xor_b32_e32 v3, 0x6e, v66
	v_cmp_gt_i32_e64 s[6:7], 0, v9
	v_or_b32_e32 v0, 16, v66
	v_xor_b32_e32 v2, 0x6f, v66
	v_cndmask_b32_e64 v1, v3, v1, s[6:7]
	v_cmp_gt_i32_e64 s[6:7], 0, v8
	v_and_b32_e32 v3, 0xffffff80, v8
	s_nop 0
	v_cndmask_b32_e64 v0, v2, v0, s[6:7]
	v_and_b32_e32 v2, 0xffffff80, v9
	v_or_b32_e32 v217, v1, v2
	v_or_b32_e32 v218, v0, v3
	v_or_b32_e32 v1, 19, v66
	v_xor_b32_e32 v3, 0x6c, v66
	v_cmp_gt_i32_e64 s[6:7], 0, v11
	v_or_b32_e32 v0, 18, v66
	v_xor_b32_e32 v2, 0x6d, v66
	v_cndmask_b32_e64 v1, v3, v1, s[6:7]
	v_cmp_gt_i32_e64 s[6:7], 0, v10
	v_and_b32_e32 v3, 0xffffff80, v10
	s_nop 0
	v_cndmask_b32_e64 v0, v2, v0, s[6:7]
	v_and_b32_e32 v2, 0xffffff80, v11
	v_or_b32_e32 v219, v1, v2
	v_or_b32_e32 v220, v0, v3
	v_or_b32_e32 v1, 25, v66
	v_xor_b32_e32 v3, 0x66, v66
	v_cmp_gt_i32_e64 s[6:7], 0, v13
	v_or_b32_e32 v0, 24, v66
	v_xor_b32_e32 v2, 0x67, v66
	v_cndmask_b32_e64 v1, v3, v1, s[6:7]
	v_cmp_gt_i32_e64 s[6:7], 0, v12
	v_and_b32_e32 v3, 0xffffff80, v12
	s_nop 0
	v_cndmask_b32_e64 v0, v2, v0, s[6:7]
	v_and_b32_e32 v2, 0xffffff80, v13
	v_or_b32_e32 v221, v1, v2
	v_or_b32_e32 v1, 27, v66
	v_cmp_gt_i32_e64 s[6:7], 0, v15
	v_or_b32_e32 v222, v0, v3
	v_and_b32_e32 v2, 0xffffff80, v15
	v_xor_b32_e32 v0, 0x64, v66
	v_cndmask_b32_e64 v0, v0, v1, s[6:7]
	v_cmp_gt_i32_e64 s[6:7], 0, v14
	v_and_b32_e32 v3, 0xffffff80, v14
	v_or_b32_e32 v223, v0, v2
	v_xor_b32_e32 v1, 0x65, v66
	v_or_b32_e32 v188, 26, v66
	v_cndmask_b32_e64 v1, v1, v188, s[6:7]
	v_or_b32_e32 v224, v1, v3
	s_waitcnt vmcnt(23)
	v_mfma_f32_32x32x16_bf16 v[0:15], v[84:87], v[44:47], 0
	s_waitcnt vmcnt(22)
	v_mfma_f32_32x32x16_bf16 v[0:15], v[88:91], v[40:43], v[0:15]
	s_waitcnt vmcnt(21)
	v_mfma_f32_32x32x16_bf16 v[0:15], v[92:95], v[36:39], v[0:15]
	s_waitcnt vmcnt(20)
	v_mfma_f32_32x32x16_bf16 v[0:15], v[96:99], v[32:35], v[0:15]
	s_waitcnt vmcnt(19)
	v_mfma_f32_32x32x16_bf16 v[0:15], v[100:103], v[28:31], v[0:15]
	s_waitcnt vmcnt(18)
	v_mfma_f32_32x32x16_bf16 v[0:15], v[104:107], v[24:27], v[0:15]
	s_waitcnt vmcnt(17)
	v_mfma_f32_32x32x16_bf16 v[0:15], v[108:111], v[20:23], v[0:15]
	s_waitcnt vmcnt(16)
	v_mfma_f32_32x32x16_bf16 v[0:15], v[112:115], v[16:19], v[0:15]
	s_nop 3
	s_nop 7
	v_cmp_gt_i32_e64 s[6:7], 0, v1
	v_and_b32_e32 v1, 0xffffff80, v1
	v_xor_b32_e32 v181, 0x5e, v66
	v_or_b32_e32 v188, 33, v66
	v_cndmask_b32_e64 v181, v181, v188, s[6:7]
	v_cmp_gt_i32_e64 s[6:7], 0, v0
	v_and_b32_e32 v0, 0xffffff80, v0
	v_or_b32_e32 v225, v181, v1
	v_xor_b32_e32 v190, 0x5f, v66
	v_or_b32_e32 v188, 32, v66
	v_cndmask_b32_e64 v190, v190, v188, s[6:7]
	v_cmp_gt_i32_e64 s[6:7], 0, v3
	v_or_b32_e32 v226, v190, v0
	v_and_b32_e32 v3, 0xffffff80, v3
	v_xor_b32_e32 v0, 0x5c, v66
	v_or_b32_e32 v188, 35, v66
	v_cndmask_b32_e64 v0, v0, v188, s[6:7]
	v_cmp_gt_i32_e64 s[6:7], 0, v2
	v_and_b32_e32 v2, 0xffffff80, v2
	v_or_b32_e32 v227, v0, v3
	v_xor_b32_e32 v1, 0x5d, v66
	v_or_b32_e32 v188, 34, v66
	v_cndmask_b32_e64 v1, v1, v188, s[6:7]
	v_cmp_gt_i32_e64 s[6:7], 0, v5
	v_or_b32_e32 v228, v1, v2
	v_and_b32_e32 v2, 0xffffff80, v5
	v_xor_b32_e32 v0, 0x56, v66
	v_or_b32_e32 v188, 41, v66
	v_cndmask_b32_e64 v0, v0, v188, s[6:7]
	v_cmp_gt_i32_e64 s[6:7], 0, v4
	v_and_b32_e32 v3, 0xffffff80, v4
	v_or_b32_e32 v229, v0, v2
	v_xor_b32_e32 v1, 0x57, v66
	v_or_b32_e32 v188, 40, v66
	v_cndmask_b32_e64 v1, v1, v188, s[6:7]
	v_cmp_gt_i32_e64 s[6:7], 0, v7
	v_or_b32_e32 v230, v1, v3
	v_and_b32_e32 v2, 0xffffff80, v7
	v_xor_b32_e32 v0, 0x54, v66
	v_or_b32_e32 v188, 43, v66
	v_cndmask_b32_e64 v0, v0, v188, s[6:7]
	v_cmp_gt_i32_e64 s[6:7], 0, v6
	v_and_b32_e32 v3, 0xffffff80, v6
	v_or_b32_e32 v231, v0, v2
	v_xor_b32_e32 v1, 0x55, v66
	v_or_b32_e32 v188, 42, v66
	v_cndmask_b32_e64 v1, v1, v188, s[6:7]
	v_cmp_gt_i32_e64 s[6:7], 0, v9
	v_or_b32_e32 v232, v1, v3
	v_and_b32_e32 v2, 0xffffff80, v9
	v_xor_b32_e32 v0, 0x4e, v66
	v_or_b32_e32 v188, 49, v66
	v_cndmask_b32_e64 v0, v0, v188, s[6:7]
	v_cmp_gt_i32_e64 s[6:7], 0, v8
	v_and_b32_e32 v3, 0xffffff80, v8
	v_or_b32_e32 v233, v0, v2
	v_xor_b32_e32 v1, 0x4f, v66
	v_or_b32_e32 v188, 48, v66
	v_cndmask_b32_e64 v1, v1, v188, s[6:7]
	v_cmp_gt_i32_e64 s[6:7], 0, v11
	v_or_b32_e32 v234, v1, v3
	v_and_b32_e32 v2, 0xffffff80, v11
	v_xor_b32_e32 v0, 0x4c, v66
	v_or_b32_e32 v188, 51, v66
	v_cndmask_b32_e64 v0, v0, v188, s[6:7]
	v_cmp_gt_i32_e64 s[6:7], 0, v10
	v_and_b32_e32 v3, 0xffffff80, v10
	v_or_b32_e32 v235, v0, v2
	v_xor_b32_e32 v1, 0x4d, v66
	v_or_b32_e32 v188, 50, v66
	v_cndmask_b32_e64 v1, v1, v188, s[6:7]
	v_cmp_gt_i32_e64 s[6:7], 0, v13
	v_or_b32_e32 v236, v1, v3
	v_and_b32_e32 v2, 0xffffff80, v13
	v_xor_b32_e32 v0, 0x46, v66
	v_or_b32_e32 v188, 57, v66
	v_cndmask_b32_e64 v0, v0, v188, s[6:7]
	v_cmp_gt_i32_e64 s[6:7], 0, v12
	v_and_b32_e32 v3, 0xffffff80, v12
	v_or_b32_e32 v237, v0, v2
	v_xor_b32_e32 v1, 0x47, v66
	v_or_b32_e32 v188, 56, v66
	v_cndmask_b32_e64 v1, v1, v188, s[6:7]
	v_cmp_gt_i32_e64 s[6:7], 0, v15
	v_or_b32_e32 v238, v1, v3
	v_and_b32_e32 v2, 0xffffff80, v15
	v_xor_b32_e32 v0, 0x44, v66
	v_or_b32_e32 v188, 59, v66
	v_cndmask_b32_e64 v0, v0, v188, s[6:7]
	v_cmp_gt_i32_e64 s[6:7], 0, v14
	v_and_b32_e32 v3, 0xffffff80, v14
	v_or_b32_e32 v239, v0, v2
	v_xor_b32_e32 v1, 0x45, v66
	v_or_b32_e32 v188, 58, v66
	v_cndmask_b32_e64 v1, v1, v188, s[6:7]
	v_or_b32_e32 v240, v1, v3
	s_waitcnt vmcnt(15)
	v_mfma_f32_32x32x16_bf16 v[0:15], v[116:119], v[44:47], 0
	s_waitcnt vmcnt(14)
	v_mfma_f32_32x32x16_bf16 v[0:15], v[120:123], v[40:43], v[0:15]
	s_waitcnt vmcnt(13)
	v_mfma_f32_32x32x16_bf16 v[0:15], v[124:127], v[36:39], v[0:15]
	s_waitcnt vmcnt(12)
	v_mfma_f32_32x32x16_bf16 v[0:15], v[128:131], v[32:35], v[0:15]
	s_waitcnt vmcnt(11)
	v_mfma_f32_32x32x16_bf16 v[0:15], v[132:135], v[28:31], v[0:15]
	s_waitcnt vmcnt(10)
	v_mfma_f32_32x32x16_bf16 v[0:15], v[136:139], v[24:27], v[0:15]
	s_waitcnt vmcnt(9)
	v_mfma_f32_32x32x16_bf16 v[0:15], v[140:143], v[20:23], v[0:15]
	s_waitcnt vmcnt(8)
	v_mfma_f32_32x32x16_bf16 v[0:15], v[152:155], v[16:19], v[0:15]
	s_nop 3
	s_nop 7
	v_cmp_gt_i32_e64 s[6:7], 0, v1
	v_and_b32_e32 v1, 0xffffff80, v1
	v_xor_b32_e32 v182, 62, v66
	v_or_b32_e32 v188, 0x41, v66
	v_cndmask_b32_e64 v182, v182, v188, s[6:7]
	v_cmp_gt_i32_e64 s[6:7], 0, v0
	v_and_b32_e32 v0, 0xffffff80, v0
	v_or_b32_e32 v182, v182, v1
	v_xor_b32_e32 v183, 63, v66
	v_or_b32_e32 v188, 64, v66
	v_cndmask_b32_e64 v183, v183, v188, s[6:7]
	v_cmp_gt_i32_e64 s[6:7], 0, v3
	v_or_b32_e32 v183, v183, v0
	v_and_b32_e32 v3, 0xffffff80, v3
	v_xor_b32_e32 v0, 60, v66
	v_or_b32_e32 v188, 0x43, v66
	v_cndmask_b32_e64 v0, v0, v188, s[6:7]
	v_cmp_gt_i32_e64 s[6:7], 0, v2
	v_and_b32_e32 v2, 0xffffff80, v2
	v_or_b32_e32 v241, v0, v3
	v_xor_b32_e32 v1, 61, v66
	v_or_b32_e32 v188, 0x42, v66
	v_cndmask_b32_e64 v1, v1, v188, s[6:7]
	v_cmp_gt_i32_e64 s[6:7], 0, v5
	v_or_b32_e32 v242, v1, v2
	v_and_b32_e32 v2, 0xffffff80, v5
	v_xor_b32_e32 v0, 54, v66
	v_or_b32_e32 v188, 0x49, v66
	v_cndmask_b32_e64 v0, v0, v188, s[6:7]
	v_cmp_gt_i32_e64 s[6:7], 0, v4
	v_and_b32_e32 v3, 0xffffff80, v4
	v_or_b32_e32 v243, v0, v2
	v_xor_b32_e32 v1, 55, v66
	v_or_b32_e32 v188, 0x48, v66
	v_cndmask_b32_e64 v1, v1, v188, s[6:7]
	v_cmp_gt_i32_e64 s[6:7], 0, v7
	v_or_b32_e32 v244, v1, v3
	v_and_b32_e32 v2, 0xffffff80, v7
	v_xor_b32_e32 v0, 52, v66
	v_or_b32_e32 v188, 0x4b, v66
	v_cndmask_b32_e64 v0, v0, v188, s[6:7]
	v_cmp_gt_i32_e64 s[6:7], 0, v6
	v_and_b32_e32 v3, 0xffffff80, v6
	v_or_b32_e32 v245, v0, v2
	v_xor_b32_e32 v1, 53, v66
	v_or_b32_e32 v188, 0x4a, v66
	v_cndmask_b32_e64 v1, v1, v188, s[6:7]
	v_cmp_gt_i32_e64 s[6:7], 0, v9
	v_or_b32_e32 v246, v1, v3
	v_and_b32_e32 v2, 0xffffff80, v9
	v_xor_b32_e32 v0, 46, v66
	v_or_b32_e32 v188, 0x51, v66
	v_cndmask_b32_e64 v0, v0, v188, s[6:7]
	v_cmp_gt_i32_e64 s[6:7], 0, v8
	v_and_b32_e32 v3, 0xffffff80, v8
	v_or_b32_e32 v247, v0, v2
	v_xor_b32_e32 v1, 47, v66
	v_or_b32_e32 v188, 0x50, v66
	v_cndmask_b32_e64 v1, v1, v188, s[6:7]
	v_cmp_gt_i32_e64 s[6:7], 0, v11
	v_or_b32_e32 v248, v1, v3
	v_and_b32_e32 v2, 0xffffff80, v11
	v_xor_b32_e32 v0, 44, v66
	v_or_b32_e32 v188, 0x53, v66
	v_cndmask_b32_e64 v0, v0, v188, s[6:7]
	v_cmp_gt_i32_e64 s[6:7], 0, v10
	v_and_b32_e32 v3, 0xffffff80, v10
	v_or_b32_e32 v249, v0, v2
	v_xor_b32_e32 v1, 45, v66
	v_or_b32_e32 v188, 0x52, v66
	v_cndmask_b32_e64 v1, v1, v188, s[6:7]
	v_cmp_gt_i32_e64 s[6:7], 0, v13
	v_or_b32_e32 v250, v1, v3
	v_and_b32_e32 v2, 0xffffff80, v13
	v_xor_b32_e32 v0, 38, v66
	v_or_b32_e32 v188, 0x59, v66
	v_cndmask_b32_e64 v0, v0, v188, s[6:7]
	v_cmp_gt_i32_e64 s[6:7], 0, v12
	v_and_b32_e32 v3, 0xffffff80, v12
	v_or_b32_e32 v251, v0, v2
	v_xor_b32_e32 v1, 39, v66
	v_or_b32_e32 v188, 0x58, v66
	v_cndmask_b32_e64 v1, v1, v188, s[6:7]
	v_cmp_gt_i32_e64 s[6:7], 0, v15
	v_or_b32_e32 v252, v1, v3
	v_and_b32_e32 v2, 0xffffff80, v15
	v_xor_b32_e32 v0, 36, v66
	v_or_b32_e32 v188, 0x5b, v66
	v_cndmask_b32_e64 v0, v0, v188, s[6:7]
	v_cmp_gt_i32_e64 s[6:7], 0, v14
	v_and_b32_e32 v3, 0xffffff80, v14
	v_or_b32_e32 v190, v0, v2
	v_xor_b32_e32 v1, 37, v66
	v_or_b32_e32 v188, 0x5a, v66
	v_cndmask_b32_e64 v1, v1, v188, s[6:7]
	v_or_b32_e32 v195, v1, v3
	s_waitcnt vmcnt(7)
	v_mfma_f32_32x32x16_bf16 v[0:15], v[156:159], v[44:47], 0
	s_waitcnt vmcnt(6)
	v_mfma_f32_32x32x16_bf16 v[0:15], v[160:163], v[40:43], v[0:15]
	s_waitcnt vmcnt(5)
	v_mfma_f32_32x32x16_bf16 v[0:15], v[164:167], v[36:39], v[0:15]
	s_waitcnt vmcnt(4)
	v_mfma_f32_32x32x16_bf16 v[0:15], v[168:171], v[32:35], v[0:15]
	s_waitcnt vmcnt(3)
	v_mfma_f32_32x32x16_bf16 v[0:15], v[48:51], v[28:31], v[0:15]
	s_waitcnt vmcnt(2)
	v_mfma_f32_32x32x16_bf16 v[0:15], v[52:55], v[24:27], v[0:15]
	s_waitcnt vmcnt(1)
	v_mfma_f32_32x32x16_bf16 v[0:15], v[56:59], v[20:23], v[0:15]
	s_waitcnt vmcnt(0)
	v_mfma_f32_32x32x16_bf16 v[0:15], v[60:63], v[16:19], v[0:15]
	s_nop 11
	v_cmp_gt_i32_e64 s[6:7], 0, v1
	v_and_b32_e32 v1, 0xffffff80, v1
	v_and_b32_e32 v18, 0xffffff80, v0
	v_xor_b32_e32 v16, 30, v66
	v_or_b32_e32 v188, 0x61, v66
	v_cndmask_b32_e64 v16, v16, v188, s[6:7]
	v_cmp_gt_i32_e64 s[6:7], 0, v0
	v_or_b32_e32 v0, v16, v1
	v_xor_b32_e32 v17, 31, v66
	v_or_b32_e32 v188, 0x60, v66
	v_cndmask_b32_e64 v17, v17, v188, s[6:7]
	v_cmp_gt_i32_e64 s[6:7], 0, v3
	v_or_b32_e32 v1, v17, v18
	v_and_b32_e32 v3, 0xffffff80, v3
	v_xor_b32_e32 v16, 28, v66
	v_or_b32_e32 v188, 0x63, v66
	v_cndmask_b32_e64 v16, v16, v188, s[6:7]
	v_cmp_gt_i32_e64 s[6:7], 0, v2
	v_and_b32_e32 v18, 0xffffff80, v2
	v_or_b32_e32 v2, v16, v3
	v_xor_b32_e32 v17, 29, v66
	v_or_b32_e32 v188, 0x62, v66
	v_cndmask_b32_e64 v17, v17, v188, s[6:7]
	v_cmp_gt_i32_e64 s[6:7], 0, v5
	v_or_b32_e32 v3, v17, v18
	v_and_b32_e32 v5, 0xffffff80, v5
	v_xor_b32_e32 v16, 22, v66
	v_or_b32_e32 v188, 0x69, v66
	v_cndmask_b32_e64 v16, v16, v188, s[6:7]
	v_cmp_gt_i32_e64 s[6:7], 0, v4
	v_and_b32_e32 v18, 0xffffff80, v4
	v_or_b32_e32 v4, v16, v5
	v_xor_b32_e32 v17, 23, v66
	v_or_b32_e32 v188, 0x68, v66
	v_cndmask_b32_e64 v17, v17, v188, s[6:7]
	v_cmp_gt_i32_e64 s[6:7], 0, v7
	v_or_b32_e32 v5, v17, v18
	v_and_b32_e32 v7, 0xffffff80, v7
	v_xor_b32_e32 v16, 20, v66
	v_or_b32_e32 v188, 0x6b, v66
	v_cndmask_b32_e64 v16, v16, v188, s[6:7]
	v_cmp_gt_i32_e64 s[6:7], 0, v6
	v_and_b32_e32 v18, 0xffffff80, v6
	v_or_b32_e32 v6, v16, v7
	v_xor_b32_e32 v17, 21, v66
	v_or_b32_e32 v188, 0x6a, v66
	v_cndmask_b32_e64 v17, v17, v188, s[6:7]
	v_cmp_gt_i32_e64 s[6:7], 0, v9
	v_or_b32_e32 v7, v17, v18
	v_and_b32_e32 v9, 0xffffff80, v9
	v_xor_b32_e32 v16, 14, v66
	v_or_b32_e32 v188, 0x71, v66
	v_cndmask_b32_e64 v16, v16, v188, s[6:7]
	v_cmp_gt_i32_e64 s[6:7], 0, v8
	v_and_b32_e32 v18, 0xffffff80, v8
	v_or_b32_e32 v8, v16, v9
	v_xor_b32_e32 v17, 15, v66
	v_or_b32_e32 v188, 0x70, v66
	v_cndmask_b32_e64 v17, v17, v188, s[6:7]
	v_cmp_gt_i32_e64 s[6:7], 0, v11
	v_or_b32_e32 v9, v17, v18
	v_and_b32_e32 v11, 0xffffff80, v11
	v_xor_b32_e32 v16, 12, v66
	v_or_b32_e32 v188, 0x73, v66
	v_cndmask_b32_e64 v16, v16, v188, s[6:7]
	v_cmp_gt_i32_e64 s[6:7], 0, v10
	v_and_b32_e32 v18, 0xffffff80, v10
	v_or_b32_e32 v10, v16, v11
	v_xor_b32_e32 v17, 13, v66
	v_or_b32_e32 v188, 0x72, v66
	v_cndmask_b32_e64 v17, v17, v188, s[6:7]
	v_cmp_gt_i32_e64 s[6:7], 0, v13
	v_or_b32_e32 v11, v17, v18
	v_and_b32_e32 v13, 0xffffff80, v13
	v_xor_b32_e32 v16, 6, v66
	v_or_b32_e32 v188, 0x79, v66
	v_cndmask_b32_e64 v16, v16, v188, s[6:7]
	v_cmp_gt_i32_e64 s[6:7], 0, v12
	v_and_b32_e32 v18, 0xffffff80, v12
	v_or_b32_e32 v12, v16, v13
	v_xor_b32_e32 v17, 7, v66
	v_or_b32_e32 v188, 0x78, v66
	v_cndmask_b32_e64 v17, v17, v188, s[6:7]
	v_cmp_gt_i32_e64 s[6:7], 0, v15
	v_or_b32_e32 v16, v17, v18
	v_and_b32_e32 v15, 0xffffff80, v15
	v_xor_b32_e32 v13, 4, v66
	v_or_b32_e32 v188, 0x7b, v66
	v_cndmask_b32_e64 v13, v13, v188, s[6:7]
	v_cmp_gt_i32_e64 s[6:7], 0, v14
	v_and_b32_e32 v14, 0xffffff80, v14
	v_or_b32_e32 v25, v13, v15
	v_xor_b32_e32 v17, 5, v66
	v_or_b32_e32 v188, 0x7a, v66
	v_cndmask_b32_e64 v17, v17, v188, s[6:7]
	v_or_b32_e32 v28, v17, v14
	v_max_f32_e32 v13, v211, v210
	v_min_f32_e32 v14, v211, v210
	v_min_f32_e32 v15, v212, v173
	v_max_f32_e32 v17, v212, v173
	v_max_f32_e32 v18, v214, v213
	v_min_f32_e32 v19, v214, v213
	v_min_f32_e32 v20, v216, v215
	v_max_f32_e32 v21, v216, v215
	v_max_f32_e32 v22, v218, v217
	v_min_f32_e32 v23, v218, v217
	v_min_f32_e32 v24, v220, v219
	v_max_f32_e32 v26, v220, v219
	v_max_f32_e32 v27, v222, v221
	v_min_f32_e32 v29, v222, v221
	v_min_f32_e32 v30, v224, v223
	v_max_f32_e32 v31, v224, v223
	v_max_f32_e32 v32, v13, v15
	v_min_f32_e32 v13, v13, v15
	v_max_f32_e32 v15, v14, v17
	v_min_f32_e32 v14, v14, v17
	v_min_f32_e32 v17, v18, v20
	v_max_f32_e32 v18, v18, v20
	v_min_f32_e32 v20, v19, v21
	v_max_f32_e32 v19, v19, v21
	v_max_f32_e32 v21, v22, v24
	v_min_f32_e32 v22, v22, v24
	v_max_f32_e32 v24, v23, v26
	v_min_f32_e32 v23, v23, v26
	v_min_f32_e32 v26, v27, v30
	v_max_f32_e32 v27, v27, v30
	v_min_f32_e32 v30, v29, v31
	v_max_f32_e32 v29, v29, v31
	v_max_f32_e32 v31, v32, v15
	v_min_f32_e32 v15, v32, v15
	v_max_f32_e32 v32, v13, v14
	v_min_f32_e32 v13, v13, v14
	v_min_f32_e32 v14, v17, v20
	v_max_f32_e32 v17, v17, v20
	v_min_f32_e32 v20, v18, v19
	v_max_f32_e32 v18, v18, v19
	v_max_f32_e32 v19, v21, v24
	v_min_f32_e32 v21, v21, v24
	v_max_f32_e32 v24, v22, v23
	v_min_f32_e32 v22, v22, v23
	v_min_f32_e32 v23, v26, v30
	v_max_f32_e32 v26, v26, v30
	v_min_f32_e32 v30, v27, v29
	v_max_f32_e32 v27, v27, v29
	v_max_f32_e32 v29, v31, v14
	v_min_f32_e32 v14, v31, v14
	v_max_f32_e32 v31, v15, v17
	v_min_f32_e32 v15, v15, v17
	v_max_f32_e32 v17, v32, v20
	v_min_f32_e32 v20, v32, v20
	v_max_f32_e32 v32, v13, v18
	v_min_f32_e32 v13, v13, v18
	v_min_f32_e32 v18, v19, v23
	v_max_f32_e32 v19, v19, v23
	v_min_f32_e32 v23, v21, v26
	v_max_f32_e32 v21, v21, v26
	v_min_f32_e32 v26, v24, v30
	v_max_f32_e32 v24, v24, v30
	v_min_f32_e32 v30, v22, v27
	v_max_f32_e32 v22, v22, v27
	v_max_f32_e32 v27, v29, v17
	v_min_f32_e32 v17, v29, v17
	v_max_f32_e32 v29, v31, v32
	v_min_f32_e32 v31, v31, v32
	v_max_f32_e32 v32, v14, v20
	v_min_f32_e32 v14, v14, v20
	v_max_f32_e32 v20, v15, v13
	v_min_f32_e32 v13, v15, v13
	v_min_f32_e32 v15, v18, v26
	v_max_f32_e32 v18, v18, v26
	v_min_f32_e32 v26, v23, v30
	v_max_f32_e32 v23, v23, v30
	v_min_f32_e32 v30, v19, v24
	v_max_f32_e32 v19, v19, v24
	v_min_f32_e32 v24, v21, v22
	v_max_f32_e32 v21, v21, v22
	v_max_f32_e32 v22, v27, v29
	v_min_f32_e32 v27, v27, v29
	v_max_f32_e32 v29, v17, v31
	v_min_f32_e32 v17, v17, v31
	v_max_f32_e32 v31, v32, v20
	v_min_f32_e32 v20, v32, v20
	v_max_f32_e32 v32, v14, v13
	v_min_f32_e32 v13, v14, v13
	v_min_f32_e32 v14, v15, v26
	v_max_f32_e32 v15, v15, v26
	v_min_f32_e32 v26, v18, v23
	v_max_f32_e32 v18, v18, v23
	v_min_f32_e32 v23, v30, v24
	v_max_f32_e32 v24, v30, v24
	v_min_f32_e32 v30, v19, v21
	v_max_f32_e32 v19, v19, v21
	v_max_f32_e32 v21, v22, v14
	v_min_f32_e32 v14, v22, v14
	v_max_f32_e32 v22, v27, v15
	v_min_f32_e32 v15, v27, v15
	v_max_f32_e32 v27, v29, v26
	v_min_f32_e32 v26, v29, v26
	v_max_f32_e32 v29, v17, v18
	v_min_f32_e32 v17, v17, v18
	v_max_f32_e32 v18, v31, v23
	v_min_f32_e32 v23, v31, v23
	v_max_f32_e32 v31, v20, v24
	v_min_f32_e32 v20, v20, v24
	v_max_f32_e32 v24, v32, v30
	v_min_f32_e32 v30, v32, v30
	v_max_f32_e32 v32, v13, v19
	v_min_f32_e32 v13, v13, v19
	v_max_f32_e32 v19, v21, v18
	v_min_f32_e32 v18, v21, v18
	v_max_f32_e32 v21, v22, v31
	v_min_f32_e32 v22, v22, v31
	v_max_f32_e32 v31, v27, v24
	v_min_f32_e32 v24, v27, v24
	v_max_f32_e32 v27, v29, v32
	v_min_f32_e32 v29, v29, v32
	v_max_f32_e32 v32, v14, v23
	v_min_f32_e32 v14, v14, v23
	v_max_f32_e32 v23, v15, v20
	v_min_f32_e32 v15, v15, v20
	v_max_f32_e32 v20, v26, v30
	v_min_f32_e32 v26, v26, v30
	v_max_f32_e32 v30, v17, v13
	v_min_f32_e32 v13, v17, v13
	v_max_f32_e32 v17, v19, v31
	v_min_f32_e32 v19, v19, v31
	v_max_f32_e32 v33, v21, v27
	v_min_f32_e32 v21, v21, v27
	v_max_f32_e32 v34, v18, v24
	v_min_f32_e32 v18, v18, v24
	v_max_f32_e32 v24, v22, v29
	v_min_f32_e32 v22, v22, v29
	v_max_f32_e32 v35, v32, v20
	v_min_f32_e32 v32, v32, v20
	v_max_f32_e32 v20, v23, v30
	v_min_f32_e32 v36, v23, v30
	v_max_f32_e32 v37, v14, v26
	v_min_f32_e32 v38, v14, v26
	v_max_f32_e32 v14, v15, v13
	v_min_f32_e32 v13, v15, v13
	v_max_f32_e32 v31, v17, v33
	v_min_f32_e32 v29, v17, v33
	v_max_f32_e32 v30, v19, v21
	v_min_f32_e32 v26, v19, v21
	v_max_f32_e32 v27, v34, v24
	v_min_f32_e32 v23, v34, v24
	v_max_f32_e32 v24, v18, v22
	v_min_f32_e32 v21, v18, v22
	v_max_f32_e32 v22, v35, v20
	v_min_f32_e32 v19, v35, v20
	v_max_f32_e32 v20, v32, v36
	v_min_f32_e32 v17, v32, v36
	v_max_f32_e32 v18, v37, v14
	v_min_f32_e32 v14, v37, v14
	v_max_f32_e32 v15, v38, v13
	v_min_f32_e32 v13, v38, v13
	v_max_f32_e32 v32, v226, v225
	v_min_f32_e32 v33, v226, v225
	v_min_f32_e32 v34, v228, v227
	v_max_f32_e32 v35, v228, v227
	v_max_f32_e32 v36, v230, v229
	v_min_f32_e32 v37, v230, v229
	v_min_f32_e32 v38, v232, v231
	v_max_f32_e32 v39, v232, v231
	v_max_f32_e32 v40, v234, v233
	v_min_f32_e32 v41, v234, v233
	v_min_f32_e32 v42, v236, v235
	v_max_f32_e32 v43, v236, v235
	v_max_f32_e32 v44, v238, v237
	v_min_f32_e32 v45, v238, v237
	v_min_f32_e32 v46, v240, v239
	v_max_f32_e32 v47, v240, v239
	v_max_f32_e32 v48, v32, v34
	v_min_f32_e32 v32, v32, v34
	v_max_f32_e32 v34, v33, v35
	v_min_f32_e32 v33, v33, v35
	v_min_f32_e32 v35, v36, v38
	v_max_f32_e32 v36, v36, v38
	v_min_f32_e32 v38, v37, v39
	v_max_f32_e32 v37, v37, v39
	v_max_f32_e32 v39, v40, v42
	v_min_f32_e32 v40, v40, v42
	v_max_f32_e32 v42, v41, v43
	v_min_f32_e32 v41, v41, v43
	v_min_f32_e32 v43, v44, v46
	v_max_f32_e32 v44, v44, v46
	v_min_f32_e32 v46, v45, v47
	v_max_f32_e32 v45, v45, v47
	v_max_f32_e32 v47, v48, v34
	v_min_f32_e32 v34, v48, v34
	v_max_f32_e32 v48, v32, v33
	v_min_f32_e32 v32, v32, v33
	v_min_f32_e32 v33, v35, v38
	v_max_f32_e32 v35, v35, v38
	v_min_f32_e32 v38, v36, v37
	v_max_f32_e32 v36, v36, v37
	v_max_f32_e32 v37, v39, v42
	v_min_f32_e32 v39, v39, v42
	v_max_f32_e32 v42, v40, v41
	v_min_f32_e32 v40, v40, v41
	v_min_f32_e32 v41, v43, v46
	v_max_f32_e32 v43, v43, v46
	v_min_f32_e32 v46, v44, v45
	v_max_f32_e32 v44, v44, v45
	v_max_f32_e32 v45, v47, v33
	v_min_f32_e32 v33, v47, v33
	v_max_f32_e32 v47, v34, v35
	v_min_f32_e32 v34, v34, v35
	v_max_f32_e32 v35, v48, v38
	v_min_f32_e32 v38, v48, v38
	v_max_f32_e32 v48, v32, v36
	v_min_f32_e32 v32, v32, v36
	v_min_f32_e32 v36, v37, v41
	v_max_f32_e32 v37, v37, v41
	v_min_f32_e32 v41, v39, v43
	v_max_f32_e32 v39, v39, v43
	v_min_f32_e32 v43, v42, v46
	v_max_f32_e32 v42, v42, v46
	v_min_f32_e32 v46, v40, v44
	v_max_f32_e32 v40, v40, v44
	v_max_f32_e32 v44, v45, v35
	v_min_f32_e32 v35, v45, v35
	v_max_f32_e32 v45, v47, v48
	v_min_f32_e32 v47, v47, v48
	v_max_f32_e32 v48, v33, v38
	v_min_f32_e32 v33, v33, v38
	v_max_f32_e32 v38, v34, v32
	v_min_f32_e32 v32, v34, v32
	v_min_f32_e32 v34, v36, v43
	v_max_f32_e32 v36, v36, v43
	v_min_f32_e32 v43, v41, v46
	v_max_f32_e32 v41, v41, v46
	v_min_f32_e32 v46, v37, v42
	v_max_f32_e32 v37, v37, v42
	v_min_f32_e32 v42, v39, v40
	v_max_f32_e32 v39, v39, v40
	v_max_f32_e32 v40, v44, v45
	v_min_f32_e32 v44, v44, v45
	v_max_f32_e32 v45, v35, v47
	v_min_f32_e32 v35, v35, v47
	v_max_f32_e32 v47, v48, v38
	v_min_f32_e32 v38, v48, v38
	v_max_f32_e32 v48, v33, v32
	v_min_f32_e32 v32, v33, v32
	v_min_f32_e32 v33, v34, v43
	v_max_f32_e32 v34, v34, v43
	v_min_f32_e32 v43, v36, v41
	v_max_f32_e32 v36, v36, v41
	v_min_f32_e32 v41, v46, v42
	v_max_f32_e32 v42, v46, v42
	v_min_f32_e32 v46, v37, v39
	v_max_f32_e32 v37, v37, v39
	v_max_f32_e32 v39, v40, v33
	v_min_f32_e32 v33, v40, v33
	v_max_f32_e32 v40, v44, v34
	v_min_f32_e32 v34, v44, v34
	v_max_f32_e32 v44, v45, v43
	v_min_f32_e32 v43, v45, v43
	v_max_f32_e32 v45, v35, v36
	v_min_f32_e32 v35, v35, v36
	v_max_f32_e32 v36, v47, v41
	v_min_f32_e32 v41, v47, v41
	v_max_f32_e32 v47, v38, v42
	v_min_f32_e32 v38, v38, v42
	v_max_f32_e32 v42, v48, v46
	v_min_f32_e32 v46, v48, v46
	v_max_f32_e32 v48, v32, v37
	v_min_f32_e32 v32, v32, v37
	v_max_f32_e32 v37, v39, v36
	v_min_f32_e32 v36, v39, v36
	v_max_f32_e32 v39, v40, v47
	v_min_f32_e32 v40, v40, v47
	v_max_f32_e32 v47, v44, v42
	v_min_f32_e32 v42, v44, v42
	v_max_f32_e32 v44, v45, v48
	v_min_f32_e32 v45, v45, v48
	v_max_f32_e32 v48, v33, v41
	v_min_f32_e32 v33, v33, v41
	v_max_f32_e32 v41, v34, v38
	v_min_f32_e32 v34, v34, v38
	v_max_f32_e32 v38, v43, v46
	v_min_f32_e32 v43, v43, v46
	v_max_f32_e32 v46, v35, v32
	v_min_f32_e32 v32, v35, v32
	v_max_f32_e32 v35, v37, v47
	v_min_f32_e32 v37, v37, v47
	v_max_f32_e32 v47, v39, v44
	v_min_f32_e32 v39, v39, v44
	v_max_f32_e32 v44, v36, v42
	v_min_f32_e32 v42, v36, v42
	v_max_f32_e32 v49, v40, v45
	v_min_f32_e32 v40, v40, v45
	v_max_f32_e32 v45, v48, v38
	v_min_f32_e32 v48, v48, v38
	v_max_f32_e32 v50, v41, v46
	v_min_f32_e32 v41, v41, v46
	v_max_f32_e32 v46, v33, v43
	v_min_f32_e32 v43, v33, v43
	v_max_f32_e32 v51, v34, v32
	v_min_f32_e32 v52, v34, v32
	v_max_f32_e32 v32, v35, v47
	v_min_f32_e32 v33, v35, v47
	v_max_f32_e32 v34, v37, v39
	v_min_f32_e32 v35, v37, v39
	v_max_f32_e32 v36, v44, v49
	v_min_f32_e32 v37, v44, v49
	v_max_f32_e32 v38, v42, v40
	v_min_f32_e32 v39, v42, v40
	v_max_f32_e32 v40, v45, v50
	v_min_f32_e32 v42, v45, v50
	v_max_f32_e32 v44, v48, v41
	v_min_f32_e32 v41, v48, v41
	v_max_f32_e32 v45, v46, v51
	v_min_f32_e32 v46, v46, v51
	v_max_f32_e32 v47, v43, v52
	v_min_f32_e32 v43, v43, v52
	v_max_f32_e32 v48, v183, v182
	v_min_f32_e32 v49, v183, v182
	v_min_f32_e32 v50, v242, v241
	v_max_f32_e32 v51, v242, v241
	v_max_f32_e32 v52, v244, v243
	v_min_f32_e32 v53, v244, v243
	v_min_f32_e32 v54, v246, v245
	v_max_f32_e32 v55, v246, v245
	v_max_f32_e32 v56, v248, v247
	v_min_f32_e32 v57, v248, v247
	v_min_f32_e32 v58, v250, v249
	v_max_f32_e32 v59, v250, v249
	v_max_f32_e32 v60, v252, v251
	v_min_f32_e32 v61, v252, v251
	v_min_f32_e32 v62, v195, v190
	v_max_f32_e32 v63, v195, v190
	v_max_f32_e32 v173, v48, v50
	v_min_f32_e32 v48, v48, v50
	v_max_f32_e32 v50, v49, v51
	v_min_f32_e32 v49, v49, v51
	v_min_f32_e32 v51, v52, v54
	v_max_f32_e32 v52, v52, v54
	v_min_f32_e32 v54, v53, v55
	v_max_f32_e32 v53, v53, v55
	v_max_f32_e32 v55, v56, v58
	v_min_f32_e32 v56, v56, v58
	v_max_f32_e32 v58, v57, v59
	v_min_f32_e32 v57, v57, v59
	v_min_f32_e32 v59, v60, v62
	v_max_f32_e32 v60, v60, v62
	v_min_f32_e32 v62, v61, v63
	v_max_f32_e32 v61, v61, v63
	v_max_f32_e32 v63, v173, v50
	v_min_f32_e32 v50, v173, v50
	v_max_f32_e32 v173, v48, v49
	v_min_f32_e32 v48, v48, v49
	v_min_f32_e32 v49, v51, v54
	v_max_f32_e32 v51, v51, v54
	v_min_f32_e32 v54, v52, v53
	v_max_f32_e32 v52, v52, v53
	v_max_f32_e32 v53, v55, v58
	v_min_f32_e32 v55, v55, v58
	v_max_f32_e32 v58, v56, v57
	v_min_f32_e32 v56, v56, v57
	v_min_f32_e32 v57, v59, v62
	v_max_f32_e32 v59, v59, v62
	v_min_f32_e32 v62, v60, v61
	v_max_f32_e32 v60, v60, v61
	v_max_f32_e32 v61, v63, v49
	v_min_f32_e32 v49, v63, v49
	v_max_f32_e32 v63, v50, v51
	v_min_f32_e32 v50, v50, v51
	v_max_f32_e32 v51, v173, v54
	v_min_f32_e32 v54, v173, v54
	v_max_f32_e32 v173, v48, v52
	v_min_f32_e32 v48, v48, v52
	v_min_f32_e32 v52, v53, v57
	v_max_f32_e32 v53, v53, v57
	v_min_f32_e32 v57, v55, v59
	v_max_f32_e32 v55, v55, v59
	v_min_f32_e32 v59, v58, v62
	v_max_f32_e32 v58, v58, v62
	v_min_f32_e32 v62, v56, v60
	v_max_f32_e32 v56, v56, v60
	v_max_f32_e32 v60, v61, v51
	v_min_f32_e32 v51, v61, v51
	v_max_f32_e32 v61, v63, v173
	v_min_f32_e32 v63, v63, v173
	v_max_f32_e32 v173, v49, v54
	v_min_f32_e32 v49, v49, v54
	v_max_f32_e32 v54, v50, v48
	v_min_f32_e32 v48, v50, v48
	v_min_f32_e32 v50, v52, v59
	v_max_f32_e32 v52, v52, v59
	v_min_f32_e32 v59, v57, v62
	v_max_f32_e32 v57, v57, v62
	v_min_f32_e32 v62, v53, v58
	v_max_f32_e32 v53, v53, v58
	v_min_f32_e32 v58, v55, v56
	v_max_f32_e32 v55, v55, v56
	v_max_f32_e32 v56, v60, v61
	v_min_f32_e32 v60, v60, v61
	v_max_f32_e32 v61, v51, v63
	v_min_f32_e32 v51, v51, v63
	v_max_f32_e32 v63, v173, v54
	v_min_f32_e32 v54, v173, v54
	v_max_f32_e32 v173, v49, v48
	v_min_f32_e32 v48, v49, v48
	v_min_f32_e32 v49, v50, v59
	v_max_f32_e32 v50, v50, v59
	v_min_f32_e32 v59, v52, v57
	v_max_f32_e32 v52, v52, v57
	v_min_f32_e32 v57, v62, v58
	v_max_f32_e32 v58, v62, v58
	v_min_f32_e32 v62, v53, v55
	v_max_f32_e32 v53, v53, v55
	v_max_f32_e32 v55, v56, v49
	v_min_f32_e32 v49, v56, v49
	v_max_f32_e32 v56, v60, v50
	v_min_f32_e32 v50, v60, v50
	v_max_f32_e32 v60, v61, v59
	v_min_f32_e32 v59, v61, v59
	v_max_f32_e32 v61, v51, v52
	v_min_f32_e32 v51, v51, v52
	v_max_f32_e32 v52, v63, v57
	v_min_f32_e32 v57, v63, v57
	v_max_f32_e32 v63, v54, v58
	v_min_f32_e32 v54, v54, v58
	v_max_f32_e32 v58, v173, v62
	v_min_f32_e32 v62, v173, v62
	v_max_f32_e32 v173, v48, v53
	v_min_f32_e32 v48, v48, v53
	v_max_f32_e32 v53, v55, v52
	v_min_f32_e32 v52, v55, v52
	v_max_f32_e32 v55, v56, v63
	v_min_f32_e32 v56, v56, v63
	v_max_f32_e32 v63, v60, v58
	v_min_f32_e32 v58, v60, v58
	v_max_f32_e32 v60, v61, v173
	v_min_f32_e32 v61, v61, v173
	v_max_f32_e32 v173, v49, v57
	v_min_f32_e32 v49, v49, v57
	v_max_f32_e32 v57, v50, v54
	v_min_f32_e32 v50, v50, v54
	v_max_f32_e32 v54, v59, v62
	v_min_f32_e32 v59, v59, v62
	v_max_f32_e32 v62, v51, v48
	v_min_f32_e32 v48, v51, v48
	v_max_f32_e32 v51, v53, v63
	v_min_f32_e32 v53, v53, v63
	v_max_f32_e32 v63, v55, v60
	v_min_f32_e32 v55, v55, v60
	v_max_f32_e32 v60, v52, v58
	v_min_f32_e32 v52, v52, v58
	v_max_f32_e32 v58, v56, v61
	v_min_f32_e32 v56, v56, v61
	v_max_f32_e32 v61, v173, v54
	v_min_f32_e32 v54, v173, v54
	v_max_f32_e32 v173, v57, v62
	v_min_f32_e32 v57, v57, v62
	v_max_f32_e32 v62, v49, v59
	v_min_f32_e32 v49, v49, v59
	v_max_f32_e32 v59, v50, v48
	v_min_f32_e32 v48, v50, v48
	v_max_f32_e32 v50, v51, v63
	v_min_f32_e32 v51, v51, v63
	v_max_f32_e32 v63, v53, v55
	v_min_f32_e32 v53, v53, v55
	v_max_f32_e32 v55, v60, v58
	v_min_f32_e32 v58, v60, v58
	v_max_f32_e32 v60, v52, v56
	v_min_f32_e32 v52, v52, v56
	v_max_f32_e32 v56, v61, v173
	v_min_f32_e32 v61, v61, v173
	v_max_f32_e32 v173, v54, v57
	v_min_f32_e32 v54, v54, v57
	v_max_f32_e32 v57, v62, v59
	v_min_f32_e32 v59, v62, v59
	v_max_f32_e32 v62, v49, v48
	v_min_f32_e32 v48, v49, v48
	v_max_f32_e32 v49, v1, v0
	v_min_f32_e32 v0, v1, v0
	v_min_f32_e32 v1, v3, v2
	v_max_f32_e32 v2, v3, v2
	v_max_f32_e32 v3, v5, v4
	v_min_f32_e32 v4, v5, v4
	v_min_f32_e32 v5, v7, v6
	v_max_f32_e32 v6, v7, v6
	v_max_f32_e32 v7, v9, v8
	v_min_f32_e32 v8, v9, v8
	v_min_f32_e32 v9, v11, v10
	v_max_f32_e32 v10, v11, v10
	v_max_f32_e32 v11, v16, v12
	v_min_f32_e32 v12, v16, v12
	v_min_f32_e32 v16, v28, v25
	v_max_f32_e32 v25, v28, v25
	v_max_f32_e32 v28, v49, v1
	v_min_f32_e32 v1, v49, v1
	v_max_f32_e32 v49, v0, v2
	v_min_f32_e32 v0, v0, v2
	v_min_f32_e32 v2, v3, v5
	v_max_f32_e32 v3, v3, v5
	v_min_f32_e32 v5, v4, v6
	v_max_f32_e32 v4, v4, v6
	v_max_f32_e32 v6, v7, v9
	v_min_f32_e32 v7, v7, v9
	v_max_f32_e32 v9, v8, v10
	v_min_f32_e32 v8, v8, v10
	v_min_f32_e32 v10, v11, v16
	v_max_f32_e32 v11, v11, v16
	v_min_f32_e32 v16, v12, v25
	v_max_f32_e32 v12, v12, v25
	v_max_f32_e32 v25, v28, v49
	v_min_f32_e32 v28, v28, v49
	v_max_f32_e32 v49, v1, v0
	v_min_f32_e32 v0, v1, v0
	v_min_f32_e32 v1, v2, v5
	v_max_f32_e32 v2, v2, v5
	v_min_f32_e32 v5, v3, v4
	v_max_f32_e32 v3, v3, v4
	v_max_f32_e32 v4, v6, v9
	v_min_f32_e32 v6, v6, v9
	v_max_f32_e32 v9, v7, v8
	v_min_f32_e32 v7, v7, v8
	v_min_f32_e32 v8, v10, v16
	v_max_f32_e32 v10, v10, v16
	v_min_f32_e32 v16, v11, v12
	v_max_f32_e32 v11, v11, v12
	v_max_f32_e32 v12, v25, v1
	v_min_f32_e32 v1, v25, v1
	v_max_f32_e32 v25, v28, v2
	v_min_f32_e32 v2, v28, v2
	v_max_f32_e32 v28, v49, v5
	v_min_f32_e32 v5, v49, v5
	v_max_f32_e32 v49, v0, v3
	v_min_f32_e32 v0, v0, v3
	v_min_f32_e32 v3, v4, v8
	v_max_f32_e32 v4, v4, v8
	v_min_f32_e32 v8, v6, v10
	v_max_f32_e32 v6, v6, v10
	v_min_f32_e32 v10, v9, v16
	v_max_f32_e32 v9, v9, v16
	v_min_f32_e32 v16, v7, v11
	v_max_f32_e32 v7, v7, v11
	v_max_f32_e32 v11, v12, v28
	v_min_f32_e32 v12, v12, v28
	v_max_f32_e32 v28, v25, v49
	v_min_f32_e32 v25, v25, v49
	v_max_f32_e32 v49, v1, v5
	v_min_f32_e32 v1, v1, v5
	v_max_f32_e32 v5, v2, v0
	v_min_f32_e32 v0, v2, v0
	v_min_f32_e32 v2, v3, v10
	v_max_f32_e32 v3, v3, v10
	v_min_f32_e32 v10, v8, v16
	v_max_f32_e32 v8, v8, v16
	v_min_f32_e32 v16, v4, v9
	v_max_f32_e32 v4, v4, v9
	v_min_f32_e32 v9, v6, v7
	v_max_f32_e32 v6, v6, v7
	v_max_f32_e32 v7, v11, v28
	v_min_f32_e32 v11, v11, v28
	v_max_f32_e32 v28, v12, v25
	v_min_f32_e32 v12, v12, v25
	v_max_f32_e32 v25, v49, v5
	v_min_f32_e32 v5, v49, v5
	v_max_f32_e32 v49, v1, v0
	v_min_f32_e32 v0, v1, v0
	v_min_f32_e32 v1, v2, v10
	v_max_f32_e32 v2, v2, v10
	v_min_f32_e32 v10, v3, v8
	v_max_f32_e32 v3, v3, v8
	v_min_f32_e32 v8, v16, v9
	v_max_f32_e32 v9, v16, v9
	v_min_f32_e32 v16, v4, v6
	v_max_f32_e32 v4, v4, v6
	v_max_f32_e32 v6, v7, v1
	v_min_f32_e32 v1, v7, v1
	v_max_f32_e32 v7, v11, v2
	v_min_f32_e32 v2, v11, v2
	v_max_f32_e32 v11, v28, v10
	v_min_f32_e32 v10, v28, v10
	v_max_f32_e32 v28, v12, v3
	v_min_f32_e32 v3, v12, v3
	v_max_f32_e32 v12, v25, v8
	v_min_f32_e32 v8, v25, v8
	v_max_f32_e32 v25, v5, v9
	v_min_f32_e32 v5, v5, v9
	v_max_f32_e32 v9, v49, v16
	v_min_f32_e32 v16, v49, v16
	v_max_f32_e32 v49, v0, v4
	v_min_f32_e32 v0, v0, v4
	v_max_f32_e32 v4, v6, v12
	v_min_f32_e32 v6, v6, v12
	v_max_f32_e32 v12, v7, v25
	v_min_f32_e32 v7, v7, v25
	v_max_f32_e32 v25, v11, v9
	v_min_f32_e32 v9, v11, v9
	v_max_f32_e32 v11, v28, v49
	v_min_f32_e32 v28, v28, v49
	v_max_f32_e32 v49, v1, v8
	v_min_f32_e32 v1, v1, v8
	v_max_f32_e32 v8, v2, v5
	v_min_f32_e32 v2, v2, v5
	v_max_f32_e32 v5, v10, v16
	v_min_f32_e32 v10, v10, v16
	v_max_f32_e32 v16, v3, v0
	v_min_f32_e32 v0, v3, v0
	v_max_f32_e32 v3, v4, v25
	v_min_f32_e32 v4, v4, v25
	v_max_f32_e32 v25, v12, v11
	v_min_f32_e32 v11, v12, v11
	v_max_f32_e32 v12, v6, v9
	v_min_f32_e32 v6, v6, v9
	v_max_f32_e32 v9, v7, v28
	v_min_f32_e32 v7, v7, v28
	v_max_f32_e32 v28, v49, v5
	v_min_f32_e32 v5, v49, v5
	v_max_f32_e32 v49, v8, v16
	v_min_f32_e32 v8, v8, v16
	v_max_f32_e32 v16, v1, v10
	v_min_f32_e32 v1, v1, v10
	v_max_f32_e32 v10, v2, v0
	v_min_f32_e32 v0, v2, v0
	v_max_f32_e32 v2, v3, v25
	v_min_f32_e32 v3, v3, v25
	v_max_f32_e32 v25, v4, v11
	v_min_f32_e32 v4, v4, v11
	v_max_f32_e32 v11, v12, v9
	v_min_f32_e32 v9, v12, v9
	v_max_f32_e32 v12, v6, v7
	v_min_f32_e32 v6, v6, v7
	v_max_f32_e32 v7, v28, v49
	v_min_f32_e32 v28, v28, v49
	v_max_f32_e32 v49, v5, v8
	v_min_f32_e32 v5, v5, v8
	v_max_f32_e32 v8, v16, v10
	v_min_f32_e32 v10, v16, v10
	v_max_f32_e32 v16, v1, v0
	v_min_f32_e32 v0, v1, v0
	v_max_f32_e32 v1, v31, v43
	v_max_f32_e32 v29, v29, v47
	v_max_f32_e32 v30, v30, v46
	v_max_f32_e32 v26, v26, v45
	v_max_f32_e32 v27, v27, v41
	v_max_f32_e32 v23, v23, v44
	v_max_f32_e32 v24, v24, v42
	v_max_f32_e32 v21, v21, v40
	v_max_f32_e32 v22, v22, v39
	v_max_f32_e32 v19, v19, v38
	v_max_f32_e32 v20, v20, v37
	v_max_f32_e32 v17, v17, v36
	v_max_f32_e32 v18, v18, v35
	v_max_f32_e32 v14, v14, v34
	v_max_f32_e32 v15, v15, v33
	v_max_f32_e32 v13, v13, v32
	v_max_f32_e32 v31, v1, v22
	v_min_f32_e32 v1, v1, v22
	v_max_f32_e32 v22, v29, v19
	v_min_f32_e32 v19, v29, v19
	v_max_f32_e32 v29, v30, v20
	v_min_f32_e32 v20, v30, v20
	v_max_f32_e32 v30, v26, v17
	v_min_f32_e32 v17, v26, v17
	v_max_f32_e32 v26, v27, v18
	v_min_f32_e32 v18, v27, v18
	v_max_f32_e32 v27, v23, v14
	v_min_f32_e32 v14, v23, v14
	v_max_f32_e32 v23, v24, v15
	v_min_f32_e32 v15, v24, v15
	v_max_f32_e32 v24, v21, v13
	v_min_f32_e32 v13, v21, v13
	v_max_f32_e32 v21, v31, v26
	v_min_f32_e32 v26, v31, v26
	v_max_f32_e32 v31, v22, v27
	v_min_f32_e32 v22, v22, v27
	v_max_f32_e32 v27, v29, v23
	v_min_f32_e32 v23, v29, v23
	v_max_f32_e32 v29, v30, v24
	v_min_f32_e32 v24, v30, v24
	v_max_f32_e32 v30, v1, v18
	v_min_f32_e32 v1, v1, v18
	v_max_f32_e32 v18, v19, v14
	v_min_f32_e32 v14, v19, v14
	v_max_f32_e32 v19, v20, v15
	v_min_f32_e32 v15, v20, v15
	v_max_f32_e32 v20, v17, v13
	v_min_f32_e32 v13, v17, v13
	v_max_f32_e32 v17, v21, v27
	v_min_f32_e32 v21, v21, v27
	v_max_f32_e32 v27, v31, v29
	v_min_f32_e32 v29, v31, v29
	v_max_f32_e32 v31, v26, v23
	v_min_f32_e32 v23, v26, v23
	v_max_f32_e32 v26, v22, v24
	v_min_f32_e32 v22, v22, v24
	v_max_f32_e32 v24, v30, v19
	v_min_f32_e32 v19, v30, v19
	v_max_f32_e32 v30, v18, v20
	v_min_f32_e32 v18, v18, v20
	v_max_f32_e32 v20, v1, v15
	v_min_f32_e32 v1, v1, v15
	v_max_f32_e32 v15, v14, v13
	v_min_f32_e32 v13, v14, v13
	v_max_f32_e32 v14, v17, v27
	v_min_f32_e32 v17, v17, v27
	v_max_f32_e32 v27, v21, v29
	v_min_f32_e32 v21, v21, v29
	v_max_f32_e32 v29, v31, v26
	v_min_f32_e32 v26, v31, v26
	v_max_f32_e32 v31, v23, v22
	v_min_f32_e32 v22, v23, v22
	v_max_f32_e32 v23, v24, v30
	v_min_f32_e32 v24, v24, v30
	v_max_f32_e32 v30, v19, v18
	v_min_f32_e32 v18, v19, v18
	v_max_f32_e32 v19, v20, v15
	v_min_f32_e32 v15, v20, v15
	v_max_f32_e32 v20, v1, v13
	v_min_f32_e32 v1, v1, v13
	v_max_f32_e32 v0, v50, v0
	v_max_f32_e32 v13, v51, v16
	v_max_f32_e32 v10, v63, v10
	v_max_f32_e32 v8, v53, v8
	v_max_f32_e32 v5, v55, v5
	v_max_f32_e32 v16, v58, v49
	v_max_f32_e32 v28, v60, v28
	v_max_f32_e32 v7, v52, v7
	v_max_f32_e32 v6, v56, v6
	v_max_f32_e32 v12, v61, v12
	v_max_f32_e32 v9, v173, v9
	v_max_f32_e32 v11, v54, v11
	v_max_f32_e32 v4, v57, v4
	v_max_f32_e32 v25, v59, v25
	v_max_f32_e32 v3, v62, v3
	v_max_f32_e32 v2, v48, v2
	v_max_f32_e32 v32, v0, v6
	v_min_f32_e32 v0, v0, v6
	v_max_f32_e32 v6, v13, v12
	v_min_f32_e32 v12, v13, v12
	v_max_f32_e32 v13, v10, v9
	v_min_f32_e32 v9, v10, v9
	v_max_f32_e32 v10, v8, v11
	v_min_f32_e32 v8, v8, v11
	v_max_f32_e32 v11, v5, v4
	v_min_f32_e32 v4, v5, v4
	v_max_f32_e32 v5, v16, v25
	v_min_f32_e32 v16, v16, v25
	v_max_f32_e32 v25, v28, v3
	v_min_f32_e32 v3, v28, v3
	v_max_f32_e32 v28, v7, v2
	v_min_f32_e32 v2, v7, v2
	v_max_f32_e32 v7, v32, v11
	v_min_f32_e32 v11, v32, v11
	v_max_f32_e32 v32, v6, v5
	v_min_f32_e32 v5, v6, v5
	v_max_f32_e32 v6, v13, v25
	v_min_f32_e32 v13, v13, v25
	v_max_f32_e32 v25, v10, v28
	v_min_f32_e32 v10, v10, v28
	v_max_f32_e32 v28, v0, v4
	v_min_f32_e32 v0, v0, v4
	v_max_f32_e32 v4, v12, v16
	v_min_f32_e32 v12, v12, v16
	v_max_f32_e32 v16, v9, v3
	v_min_f32_e32 v3, v9, v3
	v_max_f32_e32 v9, v8, v2
	v_min_f32_e32 v2, v8, v2
	v_max_f32_e32 v8, v7, v6
	v_min_f32_e32 v6, v7, v6
	v_max_f32_e32 v7, v32, v25
	v_min_f32_e32 v25, v32, v25
	v_max_f32_e32 v32, v11, v13
	v_min_f32_e32 v11, v11, v13
	v_max_f32_e32 v13, v5, v10
	v_min_f32_e32 v5, v5, v10
	v_max_f32_e32 v10, v28, v16
	v_min_f32_e32 v16, v28, v16
	v_max_f32_e32 v28, v4, v9
	v_min_f32_e32 v4, v4, v9
	v_max_f32_e32 v9, v0, v3
	v_min_f32_e32 v0, v0, v3
	v_max_f32_e32 v3, v12, v2
	v_min_f32_e32 v2, v12, v2
	v_max_f32_e32 v12, v8, v7
	v_min_f32_e32 v7, v8, v7
	v_max_f32_e32 v8, v6, v25
	v_min_f32_e32 v6, v6, v25
	v_max_f32_e32 v25, v32, v13
	v_min_f32_e32 v13, v32, v13
	v_max_f32_e32 v32, v11, v5
	v_min_f32_e32 v5, v11, v5
	v_max_f32_e32 v11, v10, v28
	v_min_f32_e32 v10, v10, v28
	v_max_f32_e32 v28, v16, v4
	v_min_f32_e32 v4, v16, v4
	v_max_f32_e32 v16, v9, v3
	v_min_f32_e32 v3, v9, v3
	v_max_f32_e32 v9, v0, v2
	v_min_f32_e32 v0, v0, v2
	v_max_f32_e32 v0, v14, v0
	v_max_f32_e32 v2, v17, v9
	v_max_f32_e32 v3, v27, v3
	v_max_f32_e32 v9, v21, v16
	v_max_f32_e32 v4, v29, v4
	v_max_f32_e32 v14, v26, v28
	v_max_f32_e32 v10, v31, v10
	v_max_f32_e32 v11, v22, v11
	v_max_f32_e32 v5, v23, v5
	v_max_f32_e32 v16, v24, v32
	v_max_f32_e32 v13, v30, v13
	v_max_f32_e32 v17, v18, v25
	v_max_f32_e32 v6, v19, v6
	v_max_f32_e32 v8, v15, v8
	v_max_f32_e32 v7, v20, v7
	v_max_f32_e32 v1, v1, v12
	v_max_f32_e32 v12, v0, v5
	v_min_f32_e32 v0, v0, v5
	v_max_f32_e32 v5, v2, v16
	v_min_f32_e32 v2, v2, v16
	v_max_f32_e32 v15, v3, v13
	v_min_f32_e32 v3, v3, v13
	v_max_f32_e32 v13, v9, v17
	v_min_f32_e32 v9, v9, v17
	v_max_f32_e32 v16, v4, v6
	v_min_f32_e32 v4, v4, v6
	v_max_f32_e32 v6, v14, v8
	v_min_f32_e32 v8, v14, v8
	v_max_f32_e32 v14, v10, v7
	v_min_f32_e32 v7, v10, v7
	v_max_f32_e32 v10, v11, v1
	v_min_f32_e32 v1, v11, v1
	v_max_f32_e32 v11, v12, v16
	v_min_f32_e32 v12, v12, v16
	v_max_f32_e32 v16, v5, v6
	v_min_f32_e32 v5, v5, v6
	v_max_f32_e32 v6, v15, v14
	v_min_f32_e32 v14, v15, v14
	v_max_f32_e32 v15, v13, v10
	v_min_f32_e32 v10, v13, v10
	v_max_f32_e32 v13, v0, v4
	v_min_f32_e32 v0, v0, v4
	v_max_f32_e32 v4, v2, v8
	v_min_f32_e32 v2, v2, v8
	v_max_f32_e32 v8, v3, v7
	v_min_f32_e32 v3, v3, v7
	v_max_f32_e32 v7, v9, v1
	v_min_f32_e32 v1, v9, v1
	v_max_f32_e32 v9, v11, v6
	v_min_f32_e32 v6, v11, v6
	v_max_f32_e32 v11, v16, v15
	v_min_f32_e32 v15, v16, v15
	v_max_f32_e32 v16, v12, v14
	v_min_f32_e32 v12, v12, v14
	v_max_f32_e32 v14, v5, v10
	v_min_f32_e32 v5, v5, v10
	v_max_f32_e32 v10, v13, v8
	v_min_f32_e32 v8, v13, v8
	v_max_f32_e32 v13, v4, v7
	v_min_f32_e32 v4, v4, v7
	v_max_f32_e32 v7, v0, v3
	v_min_f32_e32 v0, v0, v3
	v_max_f32_e32 v3, v2, v1
	v_min_f32_e32 v1, v2, v1
	v_max_f32_e32 v2, v9, v11
	v_min_f32_e32 v9, v9, v11
	v_max_f32_e32 v11, v6, v15
	v_min_f32_e32 v6, v6, v15
	v_max_f32_e32 v15, v16, v14
	v_min_f32_e32 v14, v16, v14
	v_max_f32_e32 v16, v12, v5
	v_min_f32_e32 v5, v12, v5
	v_max_f32_e32 v12, v10, v13
	v_min_f32_e32 v10, v10, v13
	v_max_f32_e32 v13, v8, v4
	v_min_f32_e32 v4, v8, v4
	v_max_f32_e32 v8, v7, v3
	v_min_f32_e32 v3, v7, v3
	v_max_f32_e32 v7, v0, v1
	v_min_f32_e32 v0, v0, v1
	v_mov_b32_e32 v27, v0
	s_nop 1
	v_permlane32_swap_b32 v27, v27
	v_mov_b32_e32 v29, v7
	s_nop 1
	v_permlane32_swap_b32 v29, v29
	v_mov_b32_e32 v31, v3
	s_nop 1
	v_permlane32_swap_b32 v31, v31
	v_mov_b32_e32 v30, v8
	s_nop 1
	v_permlane32_swap_b32 v30, v30
	v_mov_b32_e32 v28, v4
	s_nop 1
	v_permlane32_swap_b32 v28, v28
	v_mov_b32_e32 v26, v13
	s_nop 1
	v_permlane32_swap_b32 v26, v26
	s_waitcnt lgkmcnt(5)
	v_mov_b32_e32 v1, v2
	s_nop 1
	v_permlane32_swap_b32 v1, v1
	v_mov_b32_e32 v25, v10
	s_nop 1
	v_permlane32_swap_b32 v25, v25
	v_max_f32_e32 v2, v2, v27
	s_waitcnt lgkmcnt(6)
	v_mov_b32_e32 v17, v9
	s_nop 1
	v_permlane32_swap_b32 v17, v17
	v_mov_b32_e32 v24, v12
	s_nop 1
	v_permlane32_swap_b32 v24, v24
	v_max_f32_e32 v9, v9, v29
	s_waitcnt lgkmcnt(7)
	v_mov_b32_e32 v18, v11
	s_nop 1
	v_permlane32_swap_b32 v18, v18
	v_mov_b32_e32 v23, v5
	s_nop 1
	v_permlane32_swap_b32 v23, v23
	v_max_f32_e32 v11, v11, v31
	s_waitcnt lgkmcnt(8)
	v_mov_b32_e32 v19, v6
	s_nop 1
	v_permlane32_swap_b32 v19, v19
	v_mov_b32_e32 v22, v16
	s_nop 1
	v_permlane32_swap_b32 v22, v22
	v_max_f32_e32 v6, v6, v30
	s_waitcnt lgkmcnt(9)
	v_mov_b32_e32 v20, v15
	s_nop 1
	v_permlane32_swap_b32 v20, v20
	v_mov_b32_e32 v21, v14
	s_nop 1
	v_permlane32_swap_b32 v21, v21
	v_max_f32_e32 v15, v15, v28
	s_waitcnt lgkmcnt(10)
	v_max_f32_e32 v14, v14, v26
	s_waitcnt lgkmcnt(8)
	v_max_f32_e32 v16, v16, v25
	s_waitcnt lgkmcnt(6)
	v_max_f32_e32 v5, v5, v24
	s_waitcnt lgkmcnt(4)
	v_max_f32_e32 v12, v12, v23
	s_waitcnt lgkmcnt(2)
	v_max_f32_e32 v10, v10, v22
	s_waitcnt lgkmcnt(0)
	v_max_f32_e32 v13, v13, v21
	v_max_f32_e32 v4, v4, v20
	v_max_f32_e32 v8, v8, v19
	v_max_f32_e32 v3, v3, v18
	v_max_f32_e32 v7, v7, v17
	v_max_f32_e32 v0, v0, v1
	v_max_f32_e32 v1, v2, v12
	v_min_f32_e32 v2, v2, v12
	v_max_f32_e32 v12, v9, v10
	v_min_f32_e32 v9, v9, v10
	v_max_f32_e32 v10, v11, v13
	v_min_f32_e32 v11, v11, v13
	v_max_f32_e32 v13, v6, v4
	v_min_f32_e32 v4, v6, v4
	v_max_f32_e32 v6, v15, v8
	v_min_f32_e32 v8, v15, v8
	v_max_f32_e32 v15, v14, v3
	v_min_f32_e32 v3, v14, v3
	v_max_f32_e32 v14, v16, v7
	v_min_f32_e32 v7, v16, v7
	v_max_f32_e32 v16, v5, v0
	v_min_f32_e32 v0, v5, v0
	v_max_f32_e32 v5, v1, v6
	v_min_f32_e32 v1, v1, v6
	v_max_f32_e32 v6, v12, v15
	v_min_f32_e32 v12, v12, v15
	v_max_f32_e32 v15, v10, v14
	v_min_f32_e32 v10, v10, v14
	v_max_f32_e32 v14, v13, v16
	v_min_f32_e32 v13, v13, v16
	v_max_f32_e32 v16, v2, v8
	v_min_f32_e32 v2, v2, v8
	v_max_f32_e32 v8, v9, v3
	v_min_f32_e32 v3, v9, v3
	v_max_f32_e32 v9, v11, v7
	v_min_f32_e32 v7, v11, v7
	v_max_f32_e32 v11, v4, v0
	v_min_f32_e32 v0, v4, v0
	v_max_f32_e32 v4, v5, v15
	v_min_f32_e32 v5, v5, v15
	v_max_f32_e32 v15, v6, v14
	v_min_f32_e32 v6, v6, v14
	v_max_f32_e32 v14, v1, v10
	v_min_f32_e32 v1, v1, v10
	v_max_f32_e32 v10, v12, v13
	v_min_f32_e32 v12, v12, v13
	v_max_f32_e32 v13, v16, v9
	v_min_f32_e32 v9, v16, v9
	v_max_f32_e32 v16, v8, v11
	v_min_f32_e32 v8, v8, v11
	v_max_f32_e32 v11, v2, v7
	v_min_f32_e32 v2, v2, v7
	v_max_f32_e32 v7, v3, v0
	v_min_f32_e32 v0, v3, v0
	v_max_f32_e32 v3, v4, v15
	v_min_f32_e32 v4, v4, v15
	v_max_f32_e32 v15, v5, v6
	v_min_f32_e32 v5, v5, v6
	v_max_f32_e32 v6, v14, v10
	v_min_f32_e32 v10, v14, v10
	v_max_f32_e32 v14, v1, v12
	v_min_f32_e32 v1, v1, v12
	v_max_f32_e32 v12, v13, v16
	v_min_f32_e32 v13, v13, v16
	v_max_f32_e32 v16, v9, v8
	v_min_f32_e32 v8, v9, v8
	v_max_f32_e32 v9, v11, v7
	v_min_f32_e32 v7, v11, v7
	v_max_f32_e32 v11, v2, v0
	v_min_f32_e32 v0, v2, v0
	v_lshl_add_u32 v2, s8, 12, v207
	ds_write2st64_b32 v2, v3, v4 offset1:1
	ds_write2st64_b32 v2, v15, v5 offset0:2 offset1:3
	ds_write2st64_b32 v2, v6, v10 offset0:4 offset1:5
	ds_write2st64_b32 v2, v14, v1 offset0:6 offset1:7
	ds_write2st64_b32 v2, v12, v13 offset0:8 offset1:9
	ds_write2st64_b32 v2, v16, v8 offset0:10 offset1:11
	ds_write2st64_b32 v2, v9, v7 offset0:12 offset1:13
	ds_write2st64_b32 v2, v11, v0 offset0:14 offset1:15
	s_mov_b64 s[6:7], 0
	s_mov_b32 s8, 1
	s_cbranch_vccz .LBB0_704
	ds_read2st64_b32 v[0:1], v207 offset1:1
	ds_read2st64_b32 v[2:3], v207 offset0:2 offset1:3
	ds_read2st64_b32 v[4:5], v207 offset0:4 offset1:5
	ds_read2st64_b32 v[6:7], v207 offset0:6 offset1:7
	ds_read2st64_b32 v[16:17], v207 offset0:16 offset1:17
	ds_read2st64_b32 v[18:19], v207 offset0:18 offset1:19
	ds_read2st64_b32 v[20:21], v207 offset0:20 offset1:21
	ds_read2st64_b32 v[22:23], v207 offset0:22 offset1:23
	ds_read2st64_b32 v[8:9], v207 offset0:8 offset1:9
	ds_read2st64_b32 v[10:11], v207 offset0:10 offset1:11
	ds_read2st64_b32 v[12:13], v207 offset0:12 offset1:13
	ds_read2st64_b32 v[14:15], v207 offset0:14 offset1:15
	ds_read2st64_b32 v[24:25], v207 offset0:24 offset1:25
	ds_read2st64_b32 v[26:27], v207 offset0:26 offset1:27
	ds_read2st64_b32 v[28:29], v207 offset0:28 offset1:29
	ds_read2st64_b32 v[30:31], v207 offset0:30 offset1:31
	s_and_saveexec_b64 s[8:9], s[38:39]
	s_cbranch_execz .LBB0_696
	s_waitcnt lgkmcnt(0)
	v_and_b32_e32 v49, 0xffffff80, v30
	v_and_b32_e32 v48, 0xffffff80, v0
	v_and_b32_e32 v39, 0xffffff80, v19
	v_and_b32_e32 v38, 0xffffff80, v20
	v_pk_add_f32 v[52:53], v[38:39], v[48:49] op_sel:[1,0] op_sel_hi:[0,1]
	v_cmp_gt_i32_e32 vcc, 0, v52
	v_bfrev_b32_e32 v43, 0.5
	s_movk_i32 s12, 0xff00
	v_cndmask_b32_e64 v43, v43, 3, vcc
	v_and_b32_e32 v42, 0xffffff80, v23
	v_and_or_b32 v56, v52, s12, v43
	v_mov_b32_e32 v43, v38
	v_pk_add_f32 v[52:53], v[48:49], v[42:43] op_sel_hi:[0,1]
	v_cmp_gt_i32_e32 vcc, 0, v53
	v_mov_b32_e32 v54, 0xfb
	v_and_b32_e32 v41, 0xffffff80, v22
	v_cndmask_b32_e64 v54, v54, 4, vcc
	v_and_b32_e32 v40, 0xffffff80, v21
	v_and_or_b32 v53, v53, s12, v54
	v_cmp_gt_i32_e32 vcc, 0, v52
	v_mov_b32_e32 v54, 0xf8
	v_mov_b32_e32 v58, 0xf9
	v_cndmask_b32_e64 v57, v54, 7, vcc
	v_pk_add_f32 v[54:55], v[48:49], v[40:41] op_sel_hi:[0,1]
	v_cmp_gt_i32_e32 vcc, 0, v55
	v_mov_b32_e32 v59, 0xfa
	v_and_b32_e32 v55, 0xffffff00, v55
	v_cndmask_b32_e64 v58, v58, 6, vcc
	v_cmp_gt_i32_e32 vcc, 0, v54
	v_and_b32_e32 v54, 0xffffff00, v54
	v_and_b32_e32 v52, 0xffffff00, v52
	v_cndmask_b32_e64 v59, v59, 5, vcc
	v_or_b32_e32 v55, v58, v55
	v_or_b32_e32 v54, v59, v54
	v_or_b32_e32 v52, v57, v52
	v_writelane_b32 v255, s8, 44
	v_min_f32_e32 v57, v55, v52
	v_max_f32_e32 v58, v53, v54
	v_min_f32_e32 v53, v53, v54
	v_max_f32_e32 v52, v55, v52
	v_writelane_b32 v255, s9, 45
	v_and_b32_e32 v45, 0xffffff80, v24
	v_and_b32_e32 v44, 0xffffff80, v27
	v_min_f32_e32 v59, v58, v57
	v_min_f32_e32 v54, v53, v52
	v_max_f32_e32 v57, v58, v57
	v_max_f32_e32 v52, v53, v52
	v_pk_add_f32 v[44:45], v[48:49], v[44:45] op_sel_hi:[0,1]
	v_and_b32_e32 v47, 0xffffff80, v26
	v_min_f32_e32 v58, v57, v52
	v_max_f32_e32 v57, v57, v52
	v_cmp_gt_i32_e32 vcc, 0, v45
	v_mov_b32_e32 v52, 0xf7
	v_and_b32_e32 v46, 0xffffff80, v25
	v_cndmask_b32_e64 v52, v52, 8, vcc
	v_and_or_b32 v45, v45, s12, v52
	v_cmp_gt_i32_e32 vcc, 0, v44
	v_mov_b32_e32 v52, 0xf4
	v_pk_add_f32 v[46:47], v[48:49], v[46:47] op_sel_hi:[0,1]
	v_cndmask_b32_e64 v52, v52, 11, vcc
	v_cmp_gt_i32_e32 vcc, 0, v47
	v_mov_b32_e32 v53, 0xf5
	v_min_f32_e32 v55, v59, v54
	v_max_f32_e32 v59, v59, v54
	v_cndmask_b32_e64 v53, v53, 10, vcc
	v_cmp_gt_i32_e32 vcc, 0, v46
	v_mov_b32_e32 v54, 0xf6
	v_and_b32_e32 v47, 0xffffff00, v47
	v_cndmask_b32_e64 v54, v54, 9, vcc
	v_and_b32_e32 v46, 0xffffff00, v46
	v_and_b32_e32 v44, 0xffffff00, v44
	v_or_b32_e32 v47, v53, v47
	v_or_b32_e32 v46, v54, v46
	v_or_b32_e32 v44, v52, v44
	v_and_b32_e32 v51, 0xffffff80, v29
	v_and_b32_e32 v50, 0xffffff80, v28
	v_writelane_b32 v255, s11, 46
	v_min_f32_e32 v52, v47, v44
	v_max_f32_e32 v53, v45, v46
	v_min_f32_e32 v46, v45, v46
	v_max_f32_e32 v47, v47, v44
	v_pk_add_f32 v[44:45], v[48:49], v[50:51] op_sel_hi:[0,1]
	v_cmp_gt_i32_e64 s[10:11], 0, v45
	v_mov_b32_e32 v50, 0xf2
	v_mov_b32_e32 v51, 0xf3
	v_cndmask_b32_e64 v50, v50, 13, s[10:11]
	v_cmp_gt_i32_e64 s[10:11], 0, v44
	v_and_b32_e32 v45, 0xffffff00, v45
	v_and_b32_e32 v44, 0xffffff00, v44
	v_cndmask_b32_e64 v51, v51, 12, s[10:11]
	v_or_b32_e32 v50, v50, v45
	v_or_b32_e32 v51, v51, v44
	v_and_b32_e32 v45, 0xffffff80, v31
	v_mov_b32_e32 v44, v49
	v_pk_add_f32 v[44:45], v[48:49], v[44:45] op_sel_hi:[0,1]
	v_cmp_gt_i32_e64 s[42:43], 0, v45
	v_mov_b32_e32 v249, 0xf0
	v_mov_b32_e32 v173, 0xf1
	v_cndmask_b32_e64 v63, v249, 15, s[42:43]
	v_cmp_gt_i32_e64 s[42:43], 0, v44
	v_and_b32_e32 v45, 0xffffff00, v45
	v_and_b32_e32 v44, 0xffffff00, v44
	v_cndmask_b32_e64 v173, v173, 14, s[42:43]
	v_or_b32_e32 v45, v63, v45
	v_or_b32_e32 v44, v173, v44
	v_max_f32_e32 v62, v51, v50
	v_min_f32_e32 v63, v44, v45
	v_min_f32_e32 v50, v51, v50
	v_max_f32_e32 v44, v44, v45
	v_max_f32_e32 v54, v53, v52
	v_max_f32_e32 v60, v46, v47
	v_min_f32_e32 v173, v62, v63
	v_min_f32_e32 v45, v50, v44
	v_min_f32_e32 v51, v53, v52
	v_min_f32_e32 v46, v46, v47
	v_max_f32_e32 v52, v62, v63
	v_max_f32_e32 v44, v50, v44
	v_max_f32_e32 v61, v54, v60
	v_min_f32_e32 v178, v173, v45
	v_max_f32_e32 v47, v51, v46
	v_min_f32_e32 v50, v52, v44
	v_min_f32_e32 v54, v54, v60
	v_max_f32_e32 v45, v173, v45
	v_min_f32_e32 v46, v51, v46
	v_max_f32_e32 v44, v52, v44
	v_min_f32_e32 v179, v61, v178
	v_min_f32_e32 v53, v47, v50
	v_min_f32_e32 v60, v54, v45
	v_min_f32_e32 v52, v46, v44
	v_max_f32_e32 v61, v61, v178
	v_max_f32_e32 v47, v47, v50
	v_max_f32_e32 v45, v54, v45
	v_max_f32_e32 v44, v46, v44
	v_min_f32_e32 v62, v179, v53
	v_min_f32_e32 v63, v60, v52
	v_min_f32_e32 v50, v61, v47
	v_min_f32_e32 v46, v45, v44
	v_max_f32_e32 v53, v179, v53
	v_max_f32_e32 v52, v60, v52
	v_max_f32_e32 v47, v61, v47
	v_max_f32_e32 v44, v45, v44
	v_min_f32_e32 v60, v53, v52
	v_min_f32_e32 v61, v47, v44
	v_max_f32_e32 v52, v53, v52
	v_max_f32_e32 v53, v47, v44
	v_and_b32_e32 v44, 0xffffff80, v1
	v_add_f32_e32 v45, v39, v44
	v_min_f32_e32 v51, v62, v63
	v_min_f32_e32 v173, v50, v46
	v_max_f32_e32 v62, v62, v63
	v_max_f32_e32 v63, v50, v46
	v_cmp_gt_i32_e32 vcc, 0, v45
	v_mov_b32_e32 v46, 0xec
	v_mov_b32_e32 v47, 0xe9
	v_cndmask_b32_e64 v46, v46, 19, vcc
	v_and_or_b32 v45, v45, s12, v46
	v_pk_add_f32 v[42:43], v[44:45], v[42:43] op_sel_hi:[0,1]
	v_cmp_gt_i32_e32 vcc, 0, v43
	v_mov_b32_e32 v46, 0xeb
	v_pk_add_f32 v[40:41], v[44:45], v[40:41] op_sel_hi:[0,1]
	v_cndmask_b32_e64 v46, v46, 20, vcc
	v_and_or_b32 v43, v43, s12, v46
	v_cmp_gt_i32_e32 vcc, 0, v42
	v_mov_b32_e32 v46, 0xe8
	v_mov_b32_e32 v50, 0xea
	v_cndmask_b32_e64 v46, v46, 23, vcc
	v_cmp_gt_i32_e32 vcc, 0, v41
	v_and_b32_e32 v41, 0xffffff00, v41
	v_and_b32_e32 v42, 0xffffff00, v42
	v_cndmask_b32_e64 v47, v47, 22, vcc
	v_cmp_gt_i32_e32 vcc, 0, v40
	v_and_b32_e32 v40, 0xffffff00, v40
	v_or_b32_e32 v41, v47, v41
	v_cndmask_b32_e64 v50, v50, 21, vcc
	v_or_b32_e32 v40, v50, v40
	v_or_b32_e32 v42, v46, v42
	v_and_b32_e32 v182, 0xffffff80, v3
	v_min_f32_e32 v46, v41, v42
	v_max_f32_e32 v47, v43, v40
	v_min_f32_e32 v40, v43, v40
	v_max_f32_e32 v41, v41, v42
	v_and_b32_e32 v37, 0xffffff80, v4
	v_max_f32_e32 v43, v47, v46
	v_min_f32_e32 v42, v40, v41
	v_max_f32_e32 v40, v40, v41
	v_min_f32_e32 v50, v47, v46
	v_and_b32_e32 v46, 0xffffff80, v2
	v_and_b32_e32 v36, 0xffffff80, v18
	v_min_f32_e32 v179, v43, v40
	v_max_f32_e32 v180, v43, v40
	v_pk_add_f32 v[40:41], v[46:47], v[38:39] op_sel_hi:[0,1]
	v_cmp_gt_i32_e32 vcc, 0, v41
	v_mov_b32_e32 v38, 0xdc
	v_and_b32_e32 v35, 0xffffff80, v7
	v_cndmask_b32_e64 v38, v38, 35, vcc
	v_and_or_b32 v41, v41, s12, v38
	v_cmp_gt_i32_e32 vcc, 0, v40
	v_mov_b32_e32 v38, 0xdb
	v_and_b32_e32 v34, 0xffffff80, v17
	v_cndmask_b32_e64 v38, v38, 36, vcc
	v_and_or_b32 v181, v40, s12, v38
	v_add_f32_e32 v38, v39, v182
	v_cmp_gt_i32_e32 vcc, 0, v38
	v_mov_b32_e32 v39, 0xcc
	s_nop 0
	v_cndmask_b32_e64 v39, v39, 51, vcc
	v_and_or_b32 v54, v38, s12, v39
	v_pk_add_f32 v[38:39], v[48:49], v[36:37]
	v_min_f32_e32 v178, v50, v42
	v_cmp_gt_i32_e32 vcc, 0, v38
	v_bfrev_b32_e32 v39, -0.5
	v_max_f32_e32 v50, v50, v42
	v_cndmask_b32_e64 v39, v39, 2, vcc
	v_and_or_b32 v38, v38, s12, v39
	v_mov_b32_e32 v39, 0xed
	v_and_b32_e32 v43, 0xffffff80, v6
	v_min_f32_e32 v183, v38, v56
	v_max_f32_e32 v56, v38, v56
	v_add_f32_e32 v38, v36, v44
	v_cmp_gt_i32_e32 vcc, 0, v38
	v_and_b32_e32 v42, 0xffffff80, v5
	v_and_b32_e32 v33, 0xffffff80, v14
	v_cndmask_b32_e64 v39, v39, 18, vcc
	v_and_or_b32 v38, v38, s12, v39
	v_mov_b32_e32 v39, 0xdd
	v_and_b32_e32 v32, 0xffffff80, v16
	v_min_f32_e32 v190, v38, v45
	v_max_f32_e32 v195, v38, v45
	v_add_f32_e32 v38, v36, v46
	v_cmp_gt_i32_e32 vcc, 0, v38
	v_mov_b32_e32 v45, 0x61
	v_mov_b32_e32 v234, 0xef
	v_cndmask_b32_e64 v39, v39, 34, vcc
	v_and_or_b32 v38, v38, s12, v39
	v_mov_b32_e32 v39, 0xcd
	v_mov_b32_e32 v241, 0xdf
	v_min_f32_e32 v209, v38, v41
	v_max_f32_e32 v210, v38, v41
	v_add_f32_e32 v38, v36, v182
	v_cmp_gt_i32_e32 vcc, 0, v38
	v_mov_b32_e32 v41, 0x42
	v_mov_b32_e32 v244, 0xcf
	v_cndmask_b32_e64 v39, v39, 50, vcc
	v_and_or_b32 v40, v38, s12, v39
	v_pk_add_f32 v[38:39], v[36:37], v[36:37] op_sel:[1,0] op_sel_hi:[0,1]
	v_cmp_gt_i32_e32 vcc, 0, v38
	v_mov_b32_e32 v39, 0xbd
	v_and_b32_e32 v47, 0xffffff80, v8
	v_cndmask_b32_e32 v39, v39, v41, vcc
	v_and_or_b32 v41, v38, s12, v39
	v_pk_add_f32 v[38:39], v[48:49], v[34:35]
	v_pk_add_f32 v[48:49], v[48:49], v[32:33]
	v_cmp_gt_i32_e32 vcc, 0, v38
	v_mov_b32_e32 v39, 0xfe
	s_mov_b32 s28, 0xff61b1e6
	v_cndmask_b32_e64 v39, v39, 1, vcc
	v_and_or_b32 v211, v38, s12, v39
	v_add_f32_e32 v38, v34, v44
	v_cmp_gt_i32_e32 vcc, 0, v38
	v_mov_b32_e32 v39, 0xee
	v_add_f32_e32 v44, v32, v44
	v_cndmask_b32_e64 v39, v39, 17, vcc
	v_and_or_b32 v212, v38, s12, v39
	v_add_f32_e32 v38, v34, v46
	v_cmp_gt_i32_e32 vcc, 0, v38
	v_mov_b32_e32 v39, 0xde
	v_add_f32_e32 v46, v32, v46
	v_cndmask_b32_e64 v39, v39, 33, vcc
	v_and_or_b32 v213, v38, s12, v39
	v_add_f32_e32 v38, v34, v182
	v_cmp_gt_i32_e32 vcc, 0, v38
	v_mov_b32_e32 v39, 0xce
	v_add_f32_e32 v182, v32, v182
	v_cndmask_b32_e64 v39, v39, 49, vcc
	v_and_or_b32 v38, v38, s12, v39
	v_cmp_gt_i32_e64 s[74:75], 0, v46
	v_cmp_gt_i32_e64 s[84:85], 0, v182
	v_min_f32_e32 v219, v38, v40
	v_max_f32_e32 v220, v38, v40
	v_pk_add_f32 v[38:39], v[36:37], v[34:35] op_sel:[1,0] op_sel_hi:[0,1]
	v_cmp_gt_i32_e32 vcc, 0, v38
	v_mov_b32_e32 v39, 0xbe
	v_mov_b32_e32 v40, 0x41
	v_cndmask_b32_e32 v39, v39, v40, vcc
	v_and_or_b32 v38, v38, s12, v39
	v_mov_b32_e32 v40, v35
	v_cndmask_b32_e64 v241, v241, 32, s[74:75]
	v_min_f32_e32 v215, v38, v41
	v_max_f32_e32 v216, v38, v41
	v_pk_add_f32 v[38:39], v[34:35], v[42:43]
	v_mov_b32_e32 v41, v43
	v_pk_add_f32 v[40:41], v[34:35], v[40:41] op_sel_hi:[0,1]
	v_cmp_gt_i32_e32 vcc, 0, v38
	v_mov_b32_e32 v34, 0xae
	v_mov_b32_e32 v39, 0x51
	v_cndmask_b32_e32 v34, v34, v39, vcc
	v_cmp_gt_i32_e32 vcc, 0, v41
	v_mov_b32_e32 v39, 0x9e
	v_and_b32_e32 v38, 0xffffff00, v38
	v_cndmask_b32_e32 v39, v39, v45, vcc
	v_or_b32_e32 v218, v34, v38
	v_cmp_gt_i32_e32 vcc, 0, v40
	v_mov_b32_e32 v34, 0x8e
	v_mov_b32_e32 v38, 0x71
	v_cndmask_b32_e32 v34, v34, v38, vcc
	v_and_or_b32 v214, v40, s12, v34
	v_cmp_gt_i32_e32 vcc, 0, v48
	v_mov_b32_e32 v34, 0xff
	v_cndmask_b32_e64 v244, v244, 48, s[84:85]
	v_cndmask_b32_e64 v34, v34, 0, vcc
	v_and_or_b32 v34, v48, s12, v34
	v_and_or_b32 v46, v46, s12, v241
	v_and_or_b32 v182, v182, s12, v244
	v_max_f32_e32 v48, v34, v211
	v_min_f32_e32 v34, v34, v211
	v_max_f32_e32 v49, v48, v183
	v_max_f32_e32 v211, v34, v56
	v_min_f32_e32 v48, v48, v183
	v_min_f32_e32 v34, v34, v56
	v_max_f32_e32 v221, v49, v211
	v_max_f32_e32 v56, v48, v34
	v_min_f32_e32 v49, v49, v211
	v_min_f32_e32 v34, v48, v34
	v_max_f32_e32 v222, v221, v55
	v_max_f32_e32 v183, v56, v58
	v_max_f32_e32 v211, v49, v59
	v_max_f32_e32 v48, v34, v57
	v_min_f32_e32 v55, v221, v55
	v_min_f32_e32 v56, v56, v58
	v_min_f32_e32 v49, v49, v59
	v_min_f32_e32 v34, v34, v57
	v_max_f32_e32 v241, v46, v213
	v_max_f32_e32 v58, v55, v56
	v_max_f32_e32 v57, v49, v34
	v_min_f32_e32 v55, v55, v56
	v_min_f32_e32 v34, v49, v34
	v_min_f32_e32 v46, v46, v213
	v_max_f32_e32 v244, v181, v182
	v_max_f32_e32 v49, v55, v34
	v_min_f32_e32 v34, v55, v34
	v_cmp_gt_i32_e64 s[6:7], 0, v44
	v_min_f32_e32 v181, v181, v182
	s_nop 0
	v_cndmask_b32_e64 v234, v234, 16, s[6:7]
	v_and_or_b32 v44, v44, s12, v234
	v_max_f32_e32 v234, v44, v212
	v_min_f32_e32 v44, v44, v212
	v_max_f32_e32 v235, v234, v190
	v_max_f32_e32 v212, v44, v195
	v_min_f32_e32 v190, v234, v190
	v_min_f32_e32 v44, v44, v195
	v_max_f32_e32 v242, v241, v209
	v_max_f32_e32 v213, v46, v210
	v_min_f32_e32 v245, v244, v219
	v_min_f32_e32 v182, v181, v220
	v_min_f32_e32 v209, v241, v209
	v_min_f32_e32 v46, v46, v210
	v_max_f32_e32 v219, v244, v219
	v_max_f32_e32 v181, v181, v220
	v_max_f32_e32 v59, v58, v57
	v_min_f32_e32 v57, v58, v57
	v_max_f32_e32 v236, v235, v212
	v_max_f32_e32 v195, v190, v44
	v_min_f32_e32 v212, v235, v212
	v_min_f32_e32 v44, v190, v44
	v_max_f32_e32 v243, v242, v213
	v_min_f32_e32 v246, v245, v182
	v_max_f32_e32 v210, v209, v46
	v_min_f32_e32 v220, v219, v181
	v_min_f32_e32 v213, v242, v213
	v_max_f32_e32 v182, v245, v182
	v_min_f32_e32 v46, v209, v46
	v_max_f32_e32 v181, v219, v181
	v_max_f32_e32 v237, v236, v178
	v_max_f32_e32 v234, v195, v179
	v_max_f32_e32 v235, v212, v50
	v_max_f32_e32 v190, v44, v180
	v_min_f32_e32 v247, v243, v246
	v_min_f32_e32 v241, v210, v220
	v_min_f32_e32 v242, v213, v182
	v_min_f32_e32 v209, v46, v181
	v_min_f32_e32 v178, v236, v178
	v_min_f32_e32 v179, v195, v179
	v_min_f32_e32 v50, v212, v50
	v_min_f32_e32 v44, v44, v180
	v_max_f32_e32 v236, v243, v246
	v_max_f32_e32 v210, v210, v220
	v_max_f32_e32 v182, v213, v182
	v_max_f32_e32 v46, v46, v181
	v_max_f32_e32 v223, v222, v183
	v_max_f32_e32 v224, v211, v48
	v_min_f32_e32 v183, v222, v183
	v_min_f32_e32 v48, v211, v48
	v_max_f32_e32 v238, v237, v234
	v_max_f32_e32 v239, v235, v190
	v_min_f32_e32 v244, v247, v241
	v_min_f32_e32 v219, v242, v209
	v_max_f32_e32 v195, v178, v179
	v_max_f32_e32 v180, v50, v44
	v_min_f32_e32 v220, v236, v210
	v_min_f32_e32 v181, v182, v46
	v_min_f32_e32 v234, v237, v234
	v_min_f32_e32 v190, v235, v190
	v_max_f32_e32 v237, v247, v241
	v_max_f32_e32 v209, v242, v209
	v_min_f32_e32 v178, v178, v179
	v_min_f32_e32 v44, v50, v44
	v_max_f32_e32 v50, v236, v210
	v_max_f32_e32 v46, v182, v46
	v_max_f32_e32 v225, v223, v224
	v_max_f32_e32 v211, v183, v48
	v_min_f32_e32 v223, v223, v224
	v_min_f32_e32 v48, v183, v48
	v_max_f32_e32 v240, v238, v239
	v_min_f32_e32 v245, v244, v219
	v_max_f32_e32 v212, v195, v180
	v_min_f32_e32 v213, v220, v181
	v_max_f32_e32 v235, v234, v190
	v_min_f32_e32 v241, v237, v209
	v_max_f32_e32 v179, v178, v44
	v_min_f32_e32 v182, v50, v46
	v_min_f32_e32 v238, v238, v239
	v_max_f32_e32 v219, v244, v219
	v_min_f32_e32 v180, v195, v180
	v_max_f32_e32 v181, v220, v181
	v_min_f32_e32 v190, v234, v190
	v_max_f32_e32 v209, v237, v209
	v_min_f32_e32 v44, v178, v44
	v_max_f32_e32 v46, v50, v46
	v_max_f32_e32 v226, v225, v51
	v_max_f32_e32 v221, v59, v173
	v_max_f32_e32 v222, v211, v60
	v_max_f32_e32 v56, v49, v61
	v_max_f32_e32 v224, v223, v62
	v_max_f32_e32 v58, v57, v63
	v_max_f32_e32 v183, v48, v52
	v_max_f32_e32 v55, v34, v53
	v_min_f32_e32 v248, v240, v245
	v_min_f32_e32 v243, v212, v213
	v_min_f32_e32 v242, v235, v241
	v_min_f32_e32 v210, v179, v182
	v_min_f32_e32 v239, v238, v219
	v_min_f32_e32 v195, v180, v181
	v_min_f32_e32 v234, v190, v209
	v_min_f32_e32 v178, v44, v46
	v_max_f32_e32 v227, v226, v221
	v_max_f32_e32 v228, v222, v56
	v_max_f32_e32 v230, v224, v58
	v_max_f32_e32 v231, v183, v55
	v_min_f32_e32 v246, v248, v243
	v_min_f32_e32 v236, v242, v210
	v_min_f32_e32 v220, v239, v195
	v_min_f32_e32 v237, v234, v178
	v_max_f32_e32 v229, v227, v228
	v_max_f32_e32 v232, v230, v231
	v_min_f32_e32 v247, v246, v236
	v_min_f32_e32 v244, v220, v237
	v_min_f32_e32 v51, v225, v51
	v_min_f32_e32 v59, v59, v173
	v_min_f32_e32 v60, v211, v60
	v_min_f32_e32 v61, v49, v61
	v_min_f32_e32 v62, v223, v62
	v_min_f32_e32 v57, v57, v63
	v_min_f32_e32 v48, v48, v52
	v_min_f32_e32 v34, v34, v53
	v_max_f32_e32 v63, v240, v245
	v_max_f32_e32 v212, v212, v213
	v_max_f32_e32 v235, v235, v241
	v_max_f32_e32 v179, v179, v182
	v_max_f32_e32 v219, v238, v219
	v_max_f32_e32 v180, v180, v181
	v_max_f32_e32 v190, v190, v209
	v_max_f32_e32 v44, v44, v46
	v_max_f32_e32 v233, v229, v232
	v_min_f32_e32 v50, v247, v244
	v_max_f32_e32 v173, v51, v59
	v_max_f32_e32 v211, v60, v61
	v_max_f32_e32 v223, v62, v57
	v_max_f32_e32 v53, v48, v34
	v_min_f32_e32 v213, v63, v212
	v_min_f32_e32 v182, v235, v179
	v_min_f32_e32 v181, v219, v180
	v_min_f32_e32 v46, v190, v44
	v_min_f32_e32 v227, v227, v228
	v_min_f32_e32 v228, v230, v231
	v_max_f32_e32 v230, v246, v236
	v_max_f32_e32 v220, v220, v237
	v_max_f32_e32 v50, v233, v50
	v_max_f32_e32 v44, v190, v44
	v_max_f32_e32 v225, v173, v211
	v_max_f32_e32 v233, v223, v53
	v_min_f32_e32 v240, v213, v182
	v_min_f32_e32 v209, v181, v46
	v_min_f32_e32 v221, v226, v221
	v_min_f32_e32 v222, v222, v56
	v_min_f32_e32 v224, v224, v58
	v_min_f32_e32 v183, v183, v55
	v_max_f32_e32 v241, v248, v243
	v_max_f32_e32 v210, v242, v210
	v_max_f32_e32 v195, v239, v195
	v_max_f32_e32 v234, v234, v178
	v_min_f32_e32 v51, v51, v59
	v_min_f32_e32 v59, v60, v61
	v_min_f32_e32 v57, v62, v57
	v_min_f32_e32 v34, v48, v34
	v_max_f32_e32 v60, v63, v212
	v_max_f32_e32 v62, v235, v179
	v_max_f32_e32 v58, v227, v228
	v_min_f32_e32 v63, v230, v220
	v_min_f32_e32 v211, v173, v211
	v_min_f32_e32 v223, v223, v53
	v_max_f32_e32 v213, v213, v182
	v_max_f32_e32 v46, v181, v46
	v_max_f32_e32 v226, v221, v222
	v_max_f32_e32 v238, v224, v183
	v_max_f32_e32 v243, v51, v59
	v_max_f32_e32 v245, v57, v34
	v_min_f32_e32 v179, v60, v62
	v_max_f32_e32 v63, v58, v63
	v_max_f32_e32 v53, v211, v223
	v_min_f32_e32 v58, v213, v46
	v_min_f32_e32 v181, v221, v222
	v_min_f32_e32 v221, v224, v183
	v_max_f32_e32 v222, v241, v210
	v_max_f32_e32 v224, v195, v234
	v_min_f32_e32 v51, v51, v59
	v_min_f32_e32 v59, v57, v34
	v_max_f32_e32 v231, v60, v62
	v_min_f32_e32 v57, v229, v232
	v_max_f32_e32 v62, v247, v244
	v_min_f32_e32 v239, v195, v234
	v_min_f32_e32 v242, v241, v210
	v_max_f32_e32 v212, v219, v180
	v_max_f32_e32 v178, v53, v58
	v_max_f32_e32 v53, v181, v221
	v_min_f32_e32 v173, v222, v224
	v_max_f32_e32 v183, v57, v62
	v_min_f32_e32 v57, v225, v233
	v_max_f32_e32 v62, v240, v209
	v_min_f32_e32 v219, v212, v44
	v_max_f32_e32 v180, v53, v173
	v_max_f32_e32 v190, v57, v62
	v_min_f32_e32 v57, v226, v238
	v_max_f32_e32 v173, v242, v239
	v_max_f32_e32 v55, v226, v238
	v_min_f32_e32 v56, v242, v239
	v_max_f32_e32 v210, v230, v220
	v_max_f32_e32 v195, v57, v173
	v_min_f32_e32 v57, v243, v245
	v_max_f32_e32 v173, v179, v219
	v_max_f32_e32 v55, v55, v56
	v_min_f32_e32 v56, v179, v219
	v_min_f32_e32 v179, v227, v228
	v_min_f32_e32 v52, v240, v209
	v_max_f32_e32 v209, v57, v173
	v_max_f32_e32 v46, v213, v46
	v_max_f32_e32 v44, v212, v44
	v_max_f32_e32 v210, v179, v210
	v_min_f32_e32 v179, v211, v223
	v_max_f32_e32 v211, v179, v46
	v_min_f32_e32 v46, v181, v221
	v_max_f32_e32 v181, v222, v224
	v_min_f32_e32 v53, v231, v44
	v_max_f32_e32 v44, v231, v44
	v_max_f32_e32 v212, v46, v181
	v_min_f32_e32 v46, v51, v59
	v_max_f32_e32 v34, v51, v59
	v_pk_add_f32 v[36:37], v[36:37], v[32:33] op_sel:[1,0] op_sel_hi:[0,1]
	v_mov_b32_e32 v37, 0xbf
	v_max_f32_e32 v213, v46, v44
	v_cmp_gt_i32_e32 vcc, 0, v36
	v_mov_b32_e32 v221, 0x50
	v_and_b32_e32 v41, 0xffffff00, v41
	v_cndmask_b32_e64 v37, v37, 64, vcc
	v_and_or_b32 v36, v36, s12, v37
	v_or_b32_e32 v217, v39, v41
	v_max_f32_e32 v49, v225, v233
	v_max_f32_e32 v44, v54, v36
	v_min_f32_e32 v54, v54, v36
	v_pk_add_f32 v[36:37], v[32:33], v[42:43] op_sel_hi:[0,1]
	v_cmp_gt_i32_e64 s[68:69], 0, v37
	v_mov_b32_e32 v42, 0x9f
	v_mov_b32_e32 v43, 0x60
	v_cndmask_b32_e64 v42, v42, v43, s[68:69]
	v_cmp_gt_i32_e64 s[68:69], 0, v36
	v_mov_b32_e32 v43, 0xaf
	v_and_b32_e32 v37, 0xffffff00, v37
	v_cndmask_b32_e64 v43, v43, v221, s[68:69]
	v_and_b32_e32 v36, 0xffffff00, v36
	v_or_b32_e32 v37, v42, v37
	v_or_b32_e32 v36, v43, v36
	v_min_f32_e32 v42, v37, v217
	v_max_f32_e32 v43, v36, v218
	v_max_f32_e32 v37, v37, v217
	v_min_f32_e32 v36, v36, v218
	v_max_f32_e32 v46, v44, v215
	v_max_f32_e32 v219, v54, v216
	v_min_f32_e32 v221, v43, v42
	v_min_f32_e32 v217, v36, v37
	v_max_f32_e32 v42, v43, v42
	v_max_f32_e32 v36, v36, v37
	v_max_f32_e32 v220, v46, v219
	v_min_f32_e32 v44, v44, v215
	v_min_f32_e32 v54, v54, v216
	v_min_f32_e32 v219, v46, v219
	v_mov_b32_e32 v46, v35
	v_min_f32_e32 v216, v42, v36
	v_max_f32_e32 v225, v42, v36
	v_pk_add_f32 v[36:37], v[32:33], v[46:47] op_sel_hi:[0,1]
	v_and_b32_e32 v45, 0xffffff80, v9
	v_max_f32_e32 v215, v44, v54
	v_min_f32_e32 v54, v44, v54
	v_mov_b32_e32 v44, v35
	v_cmp_gt_i32_e32 vcc, 0, v37
	v_mov_b32_e32 v35, 0x7f
	v_pk_add_f32 v[42:43], v[32:33], v[44:45] op_sel_hi:[0,1]
	v_cndmask_b32_e32 v35, v35, v196, vcc
	v_cmp_gt_i32_e32 vcc, 0, v36
	v_mov_b32_e32 v47, 0x8f
	v_mov_b32_e32 v45, 0x6f
	v_cndmask_b32_e32 v44, v47, v198, vcc
	v_cmp_gt_i32_e32 vcc, 0, v43
	v_mov_b32_e32 v46, 0x90
	v_and_b32_e32 v37, 0xffffff00, v37
	v_and_b32_e32 v36, 0xffffff00, v36
	v_cndmask_b32_e32 v45, v45, v46, vcc
	v_and_b32_e32 v43, 0xffffff00, v43
	v_cmp_gt_i32_e32 vcc, 0, v42
	v_or_b32_e32 v35, v35, v37
	v_or_b32_e32 v36, v44, v36
	v_or_b32_e32 v37, v45, v43
	v_and_b32_e32 v41, 0xffffff80, v10
	v_and_b32_e32 v40, 0xffffff80, v13
	v_cndmask_b32_e32 v46, v47, v198, vcc
	v_cmp_lt_f32_e32 vcc, v37, v35
	v_cmp_lt_f32_e64 s[8:9], v214, v36
	v_and_b32_e32 v39, 0xffffff80, v12
	v_cndmask_b32_e32 v43, v35, v37, vcc
	v_cndmask_b32_e64 v45, v36, v214, s[8:9]
	v_cndmask_b32_e32 v35, v37, v35, vcc
	v_pk_add_f32 v[36:37], v[32:33], v[40:41] op_sel_hi:[0,1]
	v_cmp_gt_i32_e64 s[80:81], 0, v37
	v_mov_b32_e32 v40, 0x5f
	v_mov_b32_e32 v41, 0xa0
	v_and_b32_e32 v38, 0xffffff80, v11
	v_cndmask_b32_e64 v40, v40, v41, s[80:81]
	v_and_b32_e32 v42, 0xffffff00, v42
	v_and_or_b32 v37, v37, s12, v40
	v_cmp_gt_i32_e64 s[80:81], 0, v36
	v_mov_b32_e32 v40, 0xd0
	v_pk_add_f32 v[38:39], v[32:33], v[38:39] op_sel_hi:[0,1]
	v_or_b32_e32 v42, v46, v42
	v_cndmask_b32_e64 v40, 47, v40, s[80:81]
	v_cmp_gt_i32_e64 s[80:81], 0, v39
	v_mov_b32_e32 v41, 0xc0
	v_cndmask_b32_e64 v42, v214, v42, s[8:9]
	v_cndmask_b32_e64 v41, 63, v41, s[80:81]
	v_cmp_gt_i32_e64 s[80:81], 0, v38
	v_mov_b32_e32 v214, 0x4f
	v_mov_b32_e32 v229, 0xb0
	v_cndmask_b32_e64 v214, v214, v229, s[80:81]
	v_and_b32_e32 v39, 0xffffff00, v39
	v_and_b32_e32 v38, 0xffffff00, v38
	v_and_b32_e32 v36, 0xffffff00, v36
	v_or_b32_e32 v39, v41, v39
	v_or_b32_e32 v38, v214, v38
	v_or_b32_e32 v36, v40, v36
	v_min_f32_e32 v40, v39, v36
	v_max_f32_e32 v41, v37, v38
	v_min_f32_e32 v37, v37, v38
	v_max_f32_e32 v36, v39, v36
	v_max_f32_e32 v44, v42, v43
	v_max_f32_e32 v46, v45, v35
	v_min_f32_e32 v214, v41, v40
	v_min_f32_e32 v38, v37, v36
	v_min_f32_e32 v42, v42, v43
	v_min_f32_e32 v35, v45, v35
	v_max_f32_e32 v40, v41, v40
	v_max_f32_e32 v36, v37, v36
	v_max_f32_e32 v47, v44, v46
	v_min_f32_e32 v39, v214, v38
	v_max_f32_e32 v43, v42, v35
	v_min_f32_e32 v37, v40, v36
	v_min_f32_e32 v44, v44, v46
	v_max_f32_e32 v38, v214, v38
	v_min_f32_e32 v35, v42, v35
	v_max_f32_e32 v36, v40, v36
	v_min_f32_e32 v218, v221, v217
	v_max_f32_e32 v217, v221, v217
	v_min_f32_e32 v229, v47, v39
	v_min_f32_e32 v41, v43, v37
	v_min_f32_e32 v46, v44, v38
	v_min_f32_e32 v40, v35, v36
	v_max_f32_e32 v39, v47, v39
	v_max_f32_e32 v37, v43, v37
	v_max_f32_e32 v38, v44, v38
	v_max_f32_e32 v35, v35, v36
	v_max_f32_e32 v222, v220, v218
	v_max_f32_e32 v223, v215, v216
	v_max_f32_e32 v221, v219, v217
	v_max_f32_e32 v226, v54, v225
	v_min_f32_e32 v218, v220, v218
	v_min_f32_e32 v215, v215, v216
	v_min_f32_e32 v217, v219, v217
	v_min_f32_e32 v54, v54, v225
	v_min_f32_e32 v43, v39, v37
	v_min_f32_e32 v36, v38, v35
	v_max_f32_e32 v37, v39, v37
	v_max_f32_e32 v35, v38, v35
	v_max_f32_e32 v216, v218, v215
	v_max_f32_e32 v219, v217, v54
	v_min_f32_e32 v44, v43, v36
	v_min_f32_e32 v215, v218, v215
	v_min_f32_e32 v54, v217, v54
	v_min_f32_e32 v38, v37, v35
	v_max_f32_e32 v43, v43, v36
	v_max_f32_e32 v35, v37, v35
	v_and_b32_e32 v37, 0xffffff80, v15
	v_mov_b32_e32 v36, v33
	v_pk_add_f32 v[32:33], v[32:33], v[36:37] op_sel_hi:[0,1]
	v_mov_b32_e32 v37, 0xe0
	v_max_f32_e32 v217, v215, v54
	v_min_f32_e32 v54, v215, v54
	v_cmp_gt_i32_e64 s[76:77], 0, v33
	v_and_b32_e32 v33, 0xffffff00, v33
	s_nop 0
	v_cndmask_b32_e64 v36, 15, v249, s[76:77]
	v_cmp_gt_i32_e64 s[76:77], 0, v32
	v_and_b32_e32 v32, 0xffffff00, v32
	v_or_b32_e32 v33, v36, v33
	v_cndmask_b32_e64 v37, 31, v37, s[76:77]
	v_or_b32_e32 v32, v37, v32
	v_max_f32_e32 v36, v32, v33
	v_min_f32_e32 v32, v32, v33
	v_max_f32_e32 v37, v36, v36
	v_max_f32_e32 v33, v32, v32
	v_max_f32_e32 v37, 0xff61b1e6, v37
	v_max_f32_e32 v33, 0xff61b1e6, v33
	v_max_f32_e32 v224, v222, v223
	v_max_f32_e32 v233, v37, v33
	v_min_f32_e32 v33, v37, v33
	v_max_f32_e32 v234, 0xff61b1e6, v233
	v_max_f32_e32 v37, 0xff61b1e6, v33
	v_cmp_nlt_f32_e32 vcc, s28, v33
	v_max_f32_e32 v227, v221, v226
	v_max_f32_e32 v235, v234, v37
	v_cmp_nlt_f32_e64 s[88:89], s28, v235
	v_cndmask_b32_e32 v33, v199, v33, vcc
	v_min_f32_e32 v45, v229, v41
	v_cndmask_b32_e64 v236, v199, v235, s[88:89]
	v_cmp_nlt_f32_e64 s[88:89], s28, v233
	v_min_f32_e32 v42, v46, v40
	v_min_f32_e32 v222, v222, v223
	v_cndmask_b32_e64 v233, v199, v233, s[88:89]
	v_cmp_nlt_f32_e64 s[88:89], s28, v36
	v_min_f32_e32 v221, v221, v226
	v_max_f32_e32 v41, v229, v41
	v_cndmask_b32_e64 v36, v199, v36, s[88:89]
	v_cmp_nlt_f32_e64 s[88:89], s28, v32
	v_max_f32_e32 v40, v46, v40
	s_nop 0
	v_cndmask_b32_e64 v32, v199, v32, s[88:89]
	v_max_f32_e32 v237, v36, v32
	v_min_f32_e32 v32, v36, v32
	v_max_f32_e32 v238, v233, v237
	v_max_f32_e32 v36, v33, v32
	v_max_f32_e32 v228, v224, v227
	v_min_f32_e32 v214, v45, v42
	v_max_f32_e32 v220, v216, v219
	v_max_f32_e32 v223, v222, v221
	v_min_f32_e32 v46, v41, v40
	v_min_f32_e32 v224, v224, v227
	v_max_f32_e32 v42, v45, v42
	v_min_f32_e32 v216, v216, v219
	v_min_f32_e32 v221, v222, v221
	v_max_f32_e32 v40, v41, v40
	v_max_f32_e32 v239, v238, v36
	v_min_f32_e32 v233, v233, v237
	v_min_f32_e32 v32, v33, v32
	v_min_f32_e32 v37, v234, v37
	v_min_f32_e32 v36, v238, v36
	v_max_f32_e32 v52, v49, v52
	s_mov_b64 s[6:7], s[96:97]
	v_cmp_nlt_f32_e64 s[88:89], s28, v239
	v_cmp_nlt_f32_e64 s[76:77], s28, v37
	v_cmp_nlt_f32_e64 s[14:15], s28, v36
	v_max_f32_e32 v230, v228, v214
	v_max_f32_e32 v47, v220, v44
	v_max_f32_e32 v226, v223, v46
	v_max_f32_e32 v39, v217, v38
	v_max_f32_e32 v45, v224, v42
	v_max_f32_e32 v219, v216, v43
	v_max_f32_e32 v41, v221, v40
	v_max_f32_e32 v215, v54, v35
	v_cndmask_b32_e64 v240, v199, v239, s[88:89]
	v_max_f32_e32 v33, v233, v32
	v_cndmask_b32_e64 v234, v199, v37, s[76:77]
	v_cndmask_b32_e64 v238, v199, v36, s[14:15]
	v_min_f32_e32 v32, v233, v32
	v_cmp_nlt_f32_e64 s[88:89], s28, v33
	v_cmp_nlt_f32_e32 vcc, s28, v32
	v_max_f32_e32 v48, v243, v245
	v_max_f32_e32 v225, v230, v47
	v_max_f32_e32 v218, v226, v39
	v_max_f32_e32 v227, v45, v219
	v_max_f32_e32 v222, v41, v215
	v_min_f32_e32 v241, v236, v240
	v_cndmask_b32_e64 v237, v199, v33, s[88:89]
	v_min_f32_e32 v243, v234, v238
	v_cndmask_b32_e32 v233, v199, v32, vcc
	v_max_f32_e32 v229, v225, v218
	v_max_f32_e32 v231, v227, v222
	v_min_f32_e32 v242, v241, v237
	v_min_f32_e32 v244, v243, v233
	v_min_f32_e32 v214, v228, v214
	v_max_f32_e32 v232, v229, v231
	v_min_f32_e32 v245, v242, v244
	v_max_f32_e32 v228, 0xff61b1e6, v235
	v_max_f32_e32 v235, v239, v239
	v_max_f32_e32 v36, v36, v36
	v_min_f32_e32 v44, v220, v44
	v_min_f32_e32 v46, v223, v46
	v_min_f32_e32 v38, v217, v38
	v_min_f32_e32 v42, v224, v42
	v_min_f32_e32 v43, v216, v43
	v_min_f32_e32 v40, v221, v40
	v_min_f32_e32 v35, v54, v35
	v_max_f32_e32 v235, 0xff61b1e6, v235
	v_max_f32_e32 v33, v33, v33
	v_max_f32_e32 v37, 0xff61b1e6, v37
	v_max_f32_e32 v36, 0xff61b1e6, v36
	v_max_f32_e32 v32, v32, v32
	v_max_f32_e32 v232, v232, v245
	s_mov_b32 s36, s18
	v_max_f32_e32 v33, 0xff61b1e6, v33
	v_max_f32_e32 v32, 0xff61b1e6, v32
	v_max_f32_e32 v220, v214, v44
	v_max_f32_e32 v217, v46, v38
	v_max_f32_e32 v216, v42, v43
	v_max_f32_e32 v54, v40, v35
	v_min_f32_e32 v239, v228, v235
	v_min_f32_e32 v245, 0xff61b1e6, v33
	v_min_f32_e32 v247, v37, v36
	v_min_f32_e32 v248, 0xff61b1e6, v32
	v_max_f32_e32 v223, v220, v217
	v_max_f32_e32 v221, v216, v54
	v_min_f32_e32 v246, v239, v245
	v_min_f32_e32 v249, v247, v248
	v_min_f32_e32 v47, v230, v47
	v_max_f32_e32 v230, v236, v240
	v_cmp_ngt_f32_e64 s[16:17], s28, v237
	v_max_f32_e32 v234, v234, v238
	v_cmp_ngt_f32_e64 s[14:15], s28, v233
	v_min_f32_e32 v44, v214, v44
	v_min_f32_e32 v38, v46, v38
	v_min_f32_e32 v42, v42, v43
	v_min_f32_e32 v35, v40, v35
	v_max_f32_e32 v214, v228, v235
	v_max_f32_e32 v36, v37, v36
	v_max_f32_e32 v224, v223, v221
	v_min_f32_e32 v250, v246, v249
	v_min_f32_e32 v39, v226, v39
	v_min_f32_e32 v45, v45, v219
	v_min_f32_e32 v41, v41, v215
	v_cndmask_b32_e64 v236, v199, v237, s[16:17]
	v_cndmask_b32_e64 v238, v199, v233, s[14:15]
	v_max_f32_e32 v46, v44, v38
	v_max_f32_e32 v40, v42, v35
	v_min_f32_e32 v228, v214, v33
	v_min_f32_e32 v37, v36, v32
	v_max_f32_e32 v224, v224, v250
	v_max_f32_e32 v226, v47, v39
	v_max_f32_e32 v215, v45, v41
	v_min_f32_e32 v240, v230, v236
	v_min_f32_e32 v250, v234, v238
	v_min_f32_e32 v218, v225, v218
	v_min_f32_e32 v222, v227, v222
	v_max_f32_e32 v237, v241, v237
	v_max_f32_e32 v233, v243, v233
	v_min_f32_e32 v39, v47, v39
	v_min_f32_e32 v41, v45, v41
	v_max_f32_e32 v47, v230, v236
	v_max_f32_e32 v230, v234, v238
	v_max_f32_e32 v43, v46, v40
	v_min_f32_e32 v235, v228, v37
	v_min_f32_e32 v217, v220, v217
	v_min_f32_e32 v54, v216, v54
	v_max_f32_e32 v239, v239, v245
	v_max_f32_e32 v243, v247, v248
	v_min_f32_e32 v38, v44, v38
	v_min_f32_e32 v35, v42, v35
	v_max_f32_e32 v33, v214, v33
	v_max_f32_e32 v32, v36, v32
	v_max_f32_e32 v219, v226, v215
	v_max_f32_e32 v227, v218, v222
	v_min_f32_e32 v241, v237, v233
	v_max_f32_e32 v45, v39, v41
	v_min_f32_e32 v234, v47, v230
	v_min_f32_e32 v229, v229, v231
	v_max_f32_e32 v231, v242, v244
	v_min_f32_e32 v215, v226, v215
	v_max_f32_e32 v226, v240, v250
	v_min_f32_e32 v251, v240, v250
	v_max_f32_e32 v43, v43, v235
	v_max_f32_e32 v216, v217, v54
	v_min_f32_e32 v245, v239, v243
	v_max_f32_e32 v42, v38, v35
	v_min_f32_e32 v36, v33, v32
	v_min_f32_e32 v221, v223, v221
	v_max_f32_e32 v223, v246, v249
	v_min_f32_e32 v40, v46, v40
	v_max_f32_e32 v37, v228, v37
	v_min_f32_e32 v218, v218, v222
	v_max_f32_e32 v222, v237, v233
	v_min_f32_e32 v54, v217, v54
	v_max_f32_e32 v217, v239, v243
	v_min_f32_e32 v39, v39, v41
	v_max_f32_e32 v41, v47, v230
	v_min_f32_e32 v35, v38, v35
	v_max_f32_e32 v32, v33, v32
	v_max_f32_e32 v227, v227, v241
	v_max_f32_e32 v45, v45, v234
	v_max_f32_e32 v229, v229, v231
	v_max_f32_e32 v215, v215, v226
	v_max_f32_e32 v61, v48, v56
	v_max_f32_e32 v182, v34, v53
	v_max_f32_e32 v219, v219, v251
	v_max_f32_e32 v216, v216, v245
	v_max_f32_e32 v36, v42, v36
	v_max_f32_e32 v221, v221, v223
	v_max_f32_e32 v37, v40, v37
	v_max_f32_e32 v218, v218, v222
	v_max_f32_e32 v217, v54, v217
	v_max_f32_e32 v39, v39, v41
	v_max_f32_e32 v32, v35, v32
	v_max_f32_e32 v49, v50, v52
	v_max_f32_e32 v56, v55, v61
	v_max_f32_e32 v58, v63, v178
	v_max_f32_e32 v60, v180, v182
	v_max_f32_e32 v62, v183, v190
	v_max_f32_e32 v173, v195, v209
	v_max_f32_e32 v179, v210, v211
	v_max_f32_e32 v181, v212, v213
	v_min_f32_e32 v225, v232, v224
	v_min_f32_e32 v241, v219, v43
	v_min_f32_e32 v245, v227, v216
	v_min_f32_e32 v42, v45, v36
	v_min_f32_e32 v223, v229, v221
	v_min_f32_e32 v40, v215, v37
	v_min_f32_e32 v222, v218, v217
	v_min_f32_e32 v33, v39, v32
	v_max_f32_e32 v48, v49, v56
	v_max_f32_e32 v53, v58, v60
	v_max_f32_e32 v57, v62, v173
	v_max_f32_e32 v59, v179, v181
	v_min_f32_e32 v220, v225, v241
	v_min_f32_e32 v44, v245, v42
	v_min_f32_e32 v46, v223, v40
	v_min_f32_e32 v35, v222, v33
	v_max_f32_e32 v34, v48, v53
	v_max_f32_e32 v51, v57, v59
	v_min_f32_e32 v214, v220, v44
	v_min_f32_e32 v38, v46, v35
	v_min_f32_e32 v47, v55, v61
	v_max_f32_e32 v235, v34, v51
	v_min_f32_e32 v41, v214, v38
	v_min_f32_e32 v61, v63, v178
	v_min_f32_e32 v63, v180, v182
	v_max_f32_e32 v54, v235, v41
	v_min_f32_e32 v41, v50, v52
	v_min_f32_e32 v182, v183, v190
	v_min_f32_e32 v183, v195, v209
	v_min_f32_e32 v190, v210, v211
	v_min_f32_e32 v209, v212, v213
	v_max_f32_e32 v212, v232, v224
	v_max_f32_e32 v43, v219, v43
	v_max_f32_e32 v216, v227, v216
	v_max_f32_e32 v36, v45, v36
	v_max_f32_e32 v221, v229, v221
	v_max_f32_e32 v37, v215, v37
	v_max_f32_e32 v217, v218, v217
	v_max_f32_e32 v32, v39, v32
	v_min_f32_e32 v49, v49, v56
	v_min_f32_e32 v224, v58, v60
	v_min_f32_e32 v62, v62, v173
	v_min_f32_e32 v173, v179, v181
	v_max_f32_e32 v181, v225, v241
	v_max_f32_e32 v42, v245, v42
	v_max_f32_e32 v40, v223, v40
	v_max_f32_e32 v33, v222, v33
	v_max_f32_e32 v50, v41, v47
	v_max_f32_e32 v178, v61, v63
	v_max_f32_e32 v195, v182, v183
	v_min_f32_e32 v213, v212, v43
	v_min_f32_e32 v45, v216, v36
	v_min_f32_e32 v215, v221, v37
	v_min_f32_e32 v39, v217, v32
	v_max_f32_e32 v226, v49, v224
	v_max_f32_e32 v179, v62, v173
	v_min_f32_e32 v225, v181, v42
	v_min_f32_e32 v222, v40, v33
	v_min_f32_e32 v41, v41, v47
	v_min_f32_e32 v47, v61, v63
	v_min_f32_e32 v63, v182, v183
	v_min_f32_e32 v182, v190, v209
	v_max_f32_e32 v43, v212, v43
	v_max_f32_e32 v36, v216, v36
	v_max_f32_e32 v37, v221, v37
	v_max_f32_e32 v32, v217, v32
	v_cmp_gt_f32_e64 s[24:25], v63, v182
	v_max_f32_e32 v210, v190, v209
	v_max_f32_e32 v56, v226, v179
	v_min_f32_e32 v58, v225, v222
	v_max_f32_e32 v223, v41, v47
	v_cndmask_b32_e64 v183, v182, v63, s[24:25]
	v_min_f32_e32 v209, v43, v36
	v_min_f32_e32 v212, v37, v32
	v_max_f32_e32 v56, v56, v58
	v_max_f32_e32 v58, v223, v183
	v_min_f32_e32 v60, v209, v212
	v_min_f32_e32 v48, v48, v53
	v_min_f32_e32 v217, v57, v59
	v_max_f32_e32 v44, v220, v44
	v_max_f32_e32 v35, v46, v35
	v_max_f32_e32 v58, v58, v60
	v_max_f32_e32 v53, v48, v217
	v_min_f32_e32 v46, v44, v35
	v_max_f32_e32 v180, v50, v178
	v_min_f32_e32 v219, v213, v45
	v_min_f32_e32 v218, v215, v39
	v_max_f32_e32 v59, v53, v46
	v_min_f32_e32 v46, v50, v178
	v_min_f32_e32 v50, v195, v210
	v_max_f32_e32 v45, v213, v45
	v_max_f32_e32 v39, v215, v39
	v_min_f32_e32 v49, v49, v224
	v_max_f32_e32 v53, v46, v50
	v_min_f32_e32 v57, v45, v39
	v_min_f32_e32 v213, v62, v173
	v_max_f32_e32 v42, v181, v42
	v_max_f32_e32 v33, v40, v33
	v_max_f32_e32 v60, v53, v57
	v_cmp_gt_f32_e64 s[20:21], v49, v213
	v_max_f32_e32 v211, v195, v210
	s_nop 0
	v_cndmask_b32_e64 v57, v213, v49, s[20:21]
	v_min_f32_e32 v40, v42, v33
	v_max_f32_e32 v36, v43, v36
	v_max_f32_e32 v32, v37, v32
	v_max_f32_e32 v61, v57, v40
	v_min_f32_e32 v40, v41, v47
	v_cndmask_b32_e64 v41, v63, v182, s[24:25]
	v_cmp_gt_f32_e64 s[14:15], v40, v41
	v_min_f32_e32 v34, v34, v51
	s_nop 0
	v_cndmask_b32_e64 v47, v41, v40, s[14:15]
	v_min_f32_e32 v37, v36, v32
	s_mov_b64 s[96:97], s[6:7]
	v_max_f32_e32 v62, v47, v37
	v_max_f32_e32 v37, v214, v38
	v_max_f32_e32 v35, v44, v35
	v_min_f32_e32 v55, v219, v218
	v_max_f32_e32 v63, v34, v37
	v_min_f32_e32 v34, v180, v211
	v_max_f32_e32 v37, v219, v218
	v_max_f32_e32 v52, v180, v211
	v_max_f32_e32 v33, v42, v33
	v_max_f32_e32 v173, v34, v37
	v_min_f32_e32 v34, v226, v179
	v_max_f32_e32 v37, v225, v222
	v_max_f32_e32 v32, v36, v32
	v_max_f32_e32 v178, v34, v37
	v_min_f32_e32 v34, v223, v183
	v_max_f32_e32 v37, v209, v212
	v_max_f32_e32 v55, v52, v55
	v_max_f32_e32 v179, v34, v37
	v_min_f32_e32 v34, v48, v217
	v_max_f32_e32 v180, v34, v35
	v_min_f32_e32 v34, v46, v50
	v_max_f32_e32 v35, v45, v39
	v_max_f32_e32 v181, v34, v35
	v_cndmask_b32_e64 v34, v49, v213, s[20:21]
	v_max_f32_e32 v182, v34, v33
	v_cndmask_b32_e64 v33, v40, v41, s[14:15]
	v_min_f32_e32 v52, v54, v55
	v_min_f32_e32 v190, v56, v58
	v_max_f32_e32 v183, v33, v32
	v_min_f32_e32 v53, v59, v60
	v_min_f32_e32 v57, v61, v62
	v_min_f32_e32 v195, v63, v173
	v_min_f32_e32 v209, v178, v179
	v_min_f32_e32 v210, v180, v181
	v_min_f32_e32 v211, v182, v183
	v_min_f32_e32 v216, v52, v190
	v_min_f32_e32 v215, v53, v57
	v_min_f32_e32 v51, v195, v209
	v_min_f32_e32 v50, v210, v211
	s_movk_i32 s10, 0xff
	v_min_f32_e32 v220, v216, v215
	v_min_f32_e32 v212, v51, v50
	s_movk_i32 s8, 0x7f
	v_bitop3_b32 v35, v31, s8, v31 bitop3:0xc
	v_min_f32_e32 v32, v220, v212
	v_and_b32_e32 v33, 0xff, v32
	v_bitop3_b32 v34, v32, s10, v32 bitop3:0xc
	v_cmp_gt_i32_e64 s[6:7], 0, v32
	v_readlane_b32 s94, v255, 39
	v_readlane_b32 s95, v255, 40
	v_cndmask_b32_e64 v213, v34, v33, s[6:7]
	v_and_b32_e32 v33, 0x7f, v31
	v_cmp_gt_i32_e64 s[6:7], 0, v31
	v_and_b32_e32 v34, 15, v213
	v_lshrrev_b32_e32 v214, 4, v213
	v_cndmask_b32_e64 v31, v35, v33, s[6:7]
	v_and_b32_e32 v33, 0x7f, v30
	v_bitop3_b32 v35, v30, s8, v30 bitop3:0xc
	v_cmp_gt_i32_e64 s[6:7], 0, v30
	v_readlane_b32 s86, v255, 31
	v_readlane_b32 s82, v255, 33
	v_cndmask_b32_e64 v30, v35, v33, s[6:7]
	v_and_b32_e32 v33, 0x7f, v29
	v_bitop3_b32 v35, v29, s8, v29 bitop3:0xc
	v_cmp_gt_i32_e64 s[6:7], 0, v29
	v_readlane_b32 s84, v255, 25
	v_readlane_b32 s87, v255, 32
	v_cndmask_b32_e64 v29, v35, v33, s[6:7]
	v_and_b32_e32 v33, 0x7f, v28
	v_bitop3_b32 v35, v28, s8, v28 bitop3:0xc
	v_cmp_gt_i32_e64 s[6:7], 0, v28
	v_readlane_b32 s92, v255, 35
	v_readlane_b32 s88, v255, 29
	v_cndmask_b32_e64 v28, v35, v33, s[6:7]
	v_and_b32_e32 v33, 0x7f, v27
	v_bitop3_b32 v35, v27, s8, v27 bitop3:0xc
	v_cmp_gt_i32_e64 s[6:7], 0, v27
	v_readlane_b32 s90, v255, 27
	v_readlane_b32 s78, v255, 13
	v_cndmask_b32_e64 v27, v35, v33, s[6:7]
	v_and_b32_e32 v33, 0x7f, v26
	v_bitop3_b32 v35, v26, s8, v26 bitop3:0xc
	v_cmp_gt_i32_e64 s[6:7], 0, v26
	v_readlane_b32 s83, v255, 34
	v_readlane_b32 s74, v255, 9
	v_cndmask_b32_e64 v26, v35, v33, s[6:7]
	v_and_b32_e32 v33, 0x7f, v25
	v_bitop3_b32 v35, v25, s8, v25 bitop3:0xc
	v_cmp_gt_i32_e64 s[6:7], 0, v25
	v_readlane_b32 s85, v255, 26
	v_readlane_b32 s76, v255, 11
	v_cndmask_b32_e64 v25, v35, v33, s[6:7]
	v_and_b32_e32 v33, 0x7f, v24
	v_bitop3_b32 v35, v24, s8, v24 bitop3:0xc
	v_cmp_gt_i32_e64 s[6:7], 0, v24
	v_readlane_b32 s22, v255, 23
	v_readlane_b32 s34, v255, 17
	v_cndmask_b32_e64 v24, v35, v33, s[6:7]
	v_and_b32_e32 v33, 0x7f, v23
	v_bitop3_b32 v35, v23, s8, v23 bitop3:0xc
	v_cmp_gt_i32_e64 s[6:7], 0, v23
	v_readlane_b32 s30, v255, 15
	v_readlane_b32 s81, v255, 41
	v_cndmask_b32_e64 v23, v35, v33, s[6:7]
	v_and_b32_e32 v33, 0x7f, v22
	v_bitop3_b32 v35, v22, s8, v22 bitop3:0xc
	v_cmp_gt_i32_e64 s[6:7], 0, v22
	s_movk_i32 s87, 0x4000
	v_readlane_b32 s93, v255, 36
	v_cndmask_b32_e64 v22, v35, v33, s[6:7]
	v_and_b32_e32 v33, 0x7f, v21
	v_bitop3_b32 v35, v21, s8, v21 bitop3:0xc
	v_cmp_gt_i32_e64 s[6:7], 0, v21
	v_readlane_b32 s89, v255, 30
	v_readlane_b32 s91, v255, 28
	v_cndmask_b32_e64 v21, v35, v33, s[6:7]
	v_and_b32_e32 v33, 0x7f, v20
	v_bitop3_b32 v35, v20, s8, v20 bitop3:0xc
	v_cmp_gt_i32_e64 s[6:7], 0, v20
	v_readlane_b32 s79, v255, 14
	v_readlane_b32 s83, v255, 37
	v_cndmask_b32_e64 v20, v35, v33, s[6:7]
	v_and_b32_e32 v33, 0x7f, v19
	v_bitop3_b32 v35, v19, s8, v19 bitop3:0xc
	v_cmp_gt_i32_e64 s[6:7], 0, v19
	v_readlane_b32 s75, v255, 10
	v_readlane_b32 s85, v255, 38
	v_cndmask_b32_e64 v19, v35, v33, s[6:7]
	v_and_b32_e32 v33, 0x7f, v18
	v_bitop3_b32 v35, v18, s8, v18 bitop3:0xc
	v_cmp_gt_i32_e64 s[6:7], 0, v18
	v_readlane_b32 s77, v255, 12
	v_readlane_b32 s23, v255, 24
	v_cndmask_b32_e64 v18, v35, v33, s[6:7]
	v_and_b32_e32 v33, 0x7f, v17
	v_bitop3_b32 v35, v17, s8, v17 bitop3:0xc
	v_cmp_gt_i32_e64 s[6:7], 0, v17
	s_mov_b32 s18, s36
	s_movk_i32 s27, 0x1200
	v_cndmask_b32_e64 v17, v35, v33, s[6:7]
	v_and_b32_e32 v33, 0x7f, v16
	v_bitop3_b32 v35, v16, s8, v16 bitop3:0xc
	v_cmp_gt_i32_e64 s[6:7], 0, v16
	v_readlane_b32 s35, v255, 18
	v_readlane_b32 s31, v255, 16
	v_cndmask_b32_e64 v33, v35, v33, s[6:7]
	v_lshl_add_u32 v252, v34, 8, v207
	ds_read_b32 v16, v252 offset:4096
	v_bitop3_b32 v35, v15, s8, v15 bitop3:0xc
	s_nop 0
	s_nop 1
	s_nop 1
	s_nop 1
	s_nop 1
	s_nop 1
	s_nop 1
	s_nop 1
	s_nop 1
	s_nop 1
	s_nop 1
	s_nop 1
	s_nop 1
	s_nop 1
	s_nop 1
	v_and_b32_e32 v34, 0x7f, v15
	s_nop 0
	s_waitcnt lgkmcnt(0)
	v_and_b32_e32 v252, 0x7f, v16
	v_cmp_gt_i32_e64 s[6:7], 0, v16
	v_xor_b32_e32 v16, 0x7f, v252
	s_nop 0
	v_cndmask_b32_e64 v16, v16, v252, s[6:7]
	v_cmp_gt_i32_e64 s[6:7], 0, v15
	v_and_b32_e32 v15, 0x7f, v14
	s_nop 0
	v_cndmask_b32_e64 v34, v35, v34, s[6:7]
	v_bitop3_b32 v35, v14, s8, v14 bitop3:0xc
	v_cmp_gt_i32_e64 s[6:7], 0, v14
	v_and_b32_e32 v14, 0x7f, v13
	s_nop 0
	v_cndmask_b32_e64 v35, v35, v15, s[6:7]
	v_bitop3_b32 v15, v13, s8, v13 bitop3:0xc
	v_cmp_gt_i32_e64 s[6:7], 0, v13
	v_and_b32_e32 v13, 0x7f, v12
	s_nop 0
	v_cndmask_b32_e64 v36, v15, v14, s[6:7]
	v_bitop3_b32 v14, v12, s8, v12 bitop3:0xc
	v_cmp_gt_i32_e64 s[6:7], 0, v12
	v_and_b32_e32 v12, 0x7f, v11
	v_max_f32_e32 v15, v59, v60
	v_cndmask_b32_e64 v37, v14, v13, s[6:7]
	v_bitop3_b32 v13, v11, s8, v11 bitop3:0xc
	v_cmp_gt_i32_e64 s[6:7], 0, v11
	v_and_b32_e32 v11, 0x7f, v10
	v_max_f32_e32 v14, v56, v58
	v_cndmask_b32_e64 v38, v13, v12, s[6:7]
	v_bitop3_b32 v12, v10, s8, v10 bitop3:0xc
	v_cmp_gt_i32_e64 s[6:7], 0, v10
	v_and_b32_e32 v10, 0x7f, v9
	v_max_f32_e32 v59, v61, v62
	v_cndmask_b32_e64 v39, v12, v11, s[6:7]
	v_bitop3_b32 v11, v9, s8, v9 bitop3:0xc
	v_cmp_gt_i32_e64 s[6:7], 0, v9
	v_and_b32_e32 v9, 0x7f, v8
	v_max_f32_e32 v60, v63, v173
	v_cndmask_b32_e64 v40, v11, v10, s[6:7]
	v_bitop3_b32 v10, v8, s8, v8 bitop3:0xc
	v_cmp_gt_i32_e64 s[6:7], 0, v8
	v_and_b32_e32 v8, 0x7f, v7
	v_max_f32_e32 v61, v178, v179
	v_cndmask_b32_e64 v41, v10, v9, s[6:7]
	v_bitop3_b32 v9, v7, s8, v7 bitop3:0xc
	v_cmp_gt_i32_e64 s[6:7], 0, v7
	v_and_b32_e32 v7, 0x7f, v6
	v_max_f32_e32 v62, v180, v181
	v_cndmask_b32_e64 v42, v9, v8, s[6:7]
	v_bitop3_b32 v8, v6, s8, v6 bitop3:0xc
	v_cmp_gt_i32_e64 s[6:7], 0, v6
	v_and_b32_e32 v6, 0x7f, v5
	v_max_f32_e32 v9, v210, v211
	v_cndmask_b32_e64 v43, v8, v7, s[6:7]
	v_bitop3_b32 v7, v5, s8, v5 bitop3:0xc
	v_cmp_gt_i32_e64 s[6:7], 0, v5
	v_and_b32_e32 v5, 0x7f, v4
	v_max_f32_e32 v8, v195, v209
	v_cndmask_b32_e64 v44, v7, v6, s[6:7]
	v_bitop3_b32 v6, v4, s8, v4 bitop3:0xc
	v_cmp_gt_i32_e64 s[6:7], 0, v4
	v_and_b32_e32 v4, 0x7f, v3
	v_max_f32_e32 v63, v182, v183
	v_cndmask_b32_e64 v45, v6, v5, s[6:7]
	v_bitop3_b32 v5, v3, s8, v3 bitop3:0xc
	v_cmp_gt_i32_e64 s[6:7], 0, v3
	v_and_b32_e32 v3, 0x7f, v2
	s_nop 0
	v_cndmask_b32_e64 v46, v5, v4, s[6:7]
	v_bitop3_b32 v4, v2, s8, v2 bitop3:0xc
	v_cmp_gt_i32_e64 s[6:7], 0, v2
	v_and_b32_e32 v2, 0x7f, v1
	s_nop 0
	v_cndmask_b32_e64 v47, v4, v3, s[6:7]
	v_bitop3_b32 v3, v1, s8, v1 bitop3:0xc
	v_cmp_gt_i32_e64 s[6:7], 0, v1
	v_and_b32_e32 v1, 0x7f, v0
	v_max_f32_e32 v4, v51, v50
	v_cndmask_b32_e64 v48, v3, v2, s[6:7]
	v_bitop3_b32 v2, v0, s8, v0 bitop3:0xc
	v_cmp_gt_i32_e64 s[6:7], 0, v0
	v_min_f32_e32 v56, v60, v61
	s_nop 0
	v_cndmask_b32_e64 v49, v2, v1, s[6:7]
	v_lshl_add_u32 v252, v214, 8, v207
	ds_read_b32 v0, v252
	v_min_f32_e32 v58, v62, v63
	s_nop 0
	v_max_f32_e32 v60, v60, v61
	v_max_f32_e32 v61, v62, v63
	v_readlane_b32 s46, v255, 21
	v_readlane_b32 s44, v255, 19
	v_readlane_b32 s47, v255, 22
	v_readlane_b32 s45, v255, 20
	s_nop 1
	s_nop 1
	s_nop 1
	s_nop 1
	s_nop 1
	s_nop 1
	s_nop 1
	s_nop 1
	s_nop 1
	s_nop 1
	s_nop 1
	s_nop 1
	s_waitcnt lgkmcnt(0)
	v_and_b32_e32 v252, 0x7f, v0
	v_cmp_gt_i32_e64 s[6:7], 0, v0
	v_xor_b32_e32 v0, 0x7f, v252
	s_nop 0
	v_cndmask_b32_e64 v3, v0, v252, s[6:7]
	v_max_f32_e32 v0, v220, v212
	v_and_b32_e32 v1, 0xff, v0
	v_bitop3_b32 v2, v0, s10, v0 bitop3:0xc
	v_cmp_gt_i32_e64 s[6:7], 0, v0
	v_and_b32_e32 v12, 0xffffff00, v0
	v_lshl_add_u32 v3, v3, 7, v16
	v_cndmask_b32_e64 v0, v2, v1, s[6:7]
	v_lshrrev_b32_e32 v1, 4, v0
	v_lshl_add_u32 v252, v1, 8, v207
	ds_read_b32 v2, v252
	v_and_b32_e32 v0, 15, v0
	s_nop 0
	s_nop 1
	s_nop 1
	s_nop 1
	s_nop 1
	s_nop 1
	s_nop 1
	s_nop 1
	s_nop 1
	s_nop 1
	s_nop 1
	s_nop 1
	s_nop 1
	s_nop 1
	s_nop 1
	s_nop 1
	s_waitcnt lgkmcnt(0)
	v_and_b32_e32 v252, 0x7f, v2
	v_cmp_gt_i32_e64 s[6:7], 0, v2
	v_xor_b32_e32 v2, 0x7f, v252
	s_nop 0
	v_cndmask_b32_e64 v1, v2, v252, s[6:7]
	v_lshl_add_u32 v252, v0, 8, v207
	ds_read_b32 v2, v252 offset:4096
	s_nop 1
	s_nop 1
	s_nop 1
	s_nop 1
	s_nop 1
	s_nop 1
	s_nop 1
	s_nop 1
	s_nop 1
	s_nop 1
	s_nop 1
	s_nop 1
	s_nop 1
	s_nop 1
	s_nop 1
	s_nop 1
	s_waitcnt lgkmcnt(0)
	v_and_b32_e32 v252, 0x7f, v2
	v_cmp_gt_i32_e64 s[6:7], 0, v2
	v_xor_b32_e32 v2, 0x7f, v252
	s_nop 0
	v_cndmask_b32_e64 v0, v2, v252, s[6:7]
	v_lshl_add_u32 v2, v1, 7, v0
	v_max_f32_e32 v0, v216, v215
	v_min_f32_e32 v1, v0, v4
	v_and_b32_e32 v5, 0xff, v1
	v_bitop3_b32 v6, v1, s10, v1 bitop3:0xc
	v_cmp_gt_i32_e64 s[8:9], 0, v1
	v_and_b32_e32 v50, 0xffffff00, v1
	v_max_f32_e32 v0, v0, v4
	v_cndmask_b32_e64 v1, v6, v5, s[8:9]
	v_lshrrev_b32_e32 v5, 4, v1
	v_lshl_add_u32 v252, v5, 8, v207
	ds_read_b32 v6, v252
	v_and_b32_e32 v1, 15, v1
	v_and_b32_e32 v4, 0xff, v0
	v_cmp_gt_i32_e64 s[6:7], 0, v0
	v_and_b32_e32 v51, 0xffffff00, v0
	s_nop 1
	s_nop 1
	s_nop 1
	s_nop 1
	s_nop 1
	s_nop 1
	s_nop 1
	s_nop 1
	s_nop 1
	s_nop 1
	s_nop 1
	s_nop 1
	s_nop 1
	s_nop 1
	s_waitcnt lgkmcnt(0)
	v_and_b32_e32 v252, 0x7f, v6
	v_cmp_gt_i32_e64 s[8:9], 0, v6
	v_xor_b32_e32 v6, 0x7f, v252
	s_nop 0
	v_cndmask_b32_e64 v5, v6, v252, s[8:9]
	v_lshl_add_u32 v252, v1, 8, v207
	ds_read_b32 v6, v252 offset:4096
	s_nop 1
	s_nop 1
	s_nop 1
	s_nop 1
	s_nop 1
	s_nop 1
	s_nop 1
	s_nop 1
	s_nop 1
	s_nop 1
	s_nop 1
	s_nop 1
	s_nop 1
	s_nop 1
	s_nop 1
	s_nop 1
	s_waitcnt lgkmcnt(0)
	v_and_b32_e32 v252, 0x7f, v6
	v_cmp_gt_i32_e64 s[8:9], 0, v6
	v_xor_b32_e32 v6, 0x7f, v252
	s_nop 0
	v_cndmask_b32_e64 v1, v6, v252, s[8:9]
	v_lshl_add_u32 v1, v5, 7, v1
	v_bitop3_b32 v5, v0, s10, v0 bitop3:0xc
	v_cndmask_b32_e64 v0, v5, v4, s[6:7]
	v_lshrrev_b32_e32 v4, 4, v0
	v_lshl_add_u32 v252, v4, 8, v207
	ds_read_b32 v5, v252
	v_and_b32_e32 v0, 15, v0
	s_nop 0
	s_nop 1
	s_nop 1
	s_nop 1
	s_nop 1
	s_nop 1
	s_nop 1
	s_nop 1
	s_nop 1
	s_nop 1
	s_nop 1
	s_nop 1
	s_nop 1
	s_nop 1
	s_nop 1
	s_nop 1
	s_waitcnt lgkmcnt(0)
	v_and_b32_e32 v252, 0x7f, v5
	v_cmp_gt_i32_e64 s[6:7], 0, v5
	v_xor_b32_e32 v5, 0x7f, v252
	s_nop 0
	v_cndmask_b32_e64 v4, v5, v252, s[6:7]
	v_lshl_add_u32 v252, v0, 8, v207
	ds_read_b32 v5, v252 offset:4096
	s_nop 1
	s_nop 1
	s_nop 1
	s_nop 1
	s_nop 1
	s_nop 1
	s_nop 1
	s_nop 1
	s_nop 1
	s_nop 1
	s_nop 1
	s_nop 1
	s_nop 1
	s_nop 1
	s_nop 1
	s_nop 1
	s_waitcnt lgkmcnt(0)
	v_and_b32_e32 v252, 0x7f, v5
	v_cmp_gt_i32_e64 s[6:7], 0, v5
	v_xor_b32_e32 v5, 0x7f, v252
	s_nop 0
	v_cndmask_b32_e64 v0, v5, v252, s[6:7]
	v_lshl_add_u32 v0, v4, 7, v0
	v_max_f32_e32 v4, v52, v190
	v_max_f32_e32 v5, v53, v57
	v_min_f32_e32 v6, v4, v5
	v_min_f32_e32 v10, v8, v9
	v_max_f32_e32 v4, v4, v5
	v_max_f32_e32 v8, v8, v9
	v_min_f32_e32 v7, v6, v10
	v_and_b32_e32 v11, 0xff, v7
	v_bitop3_b32 v13, v7, s10, v7 bitop3:0xc
	v_cmp_gt_i32_e64 s[8:9], 0, v7
	v_and_b32_e32 v52, 0xffffff00, v7
	v_max_f32_e32 v6, v6, v10
	v_cndmask_b32_e64 v7, v13, v11, s[8:9]
	v_lshrrev_b32_e32 v11, 4, v7
	v_lshl_add_u32 v252, v11, 8, v207
	ds_read_b32 v13, v252
	v_and_b32_e32 v7, 15, v7
	v_and_b32_e32 v10, 0xff, v6
	v_cmp_gt_i32_e64 s[6:7], 0, v6
	v_and_b32_e32 v53, 0xffffff00, v6
	s_nop 1
	s_nop 1
	s_nop 1
	s_nop 1
	s_nop 1
	s_nop 1
	s_nop 1
	s_nop 1
	s_nop 1
	s_nop 1
	s_nop 1
	s_nop 1
	s_nop 1
	s_nop 1
	s_waitcnt lgkmcnt(0)
	v_and_b32_e32 v252, 0x7f, v13
	v_cmp_gt_i32_e64 s[8:9], 0, v13
	v_xor_b32_e32 v13, 0x7f, v252
	s_nop 0
	v_cndmask_b32_e64 v11, v13, v252, s[8:9]
	v_lshl_add_u32 v252, v7, 8, v207
	ds_read_b32 v13, v252 offset:4096
	s_nop 1
	s_nop 1
	s_nop 1
	s_nop 1
	s_nop 1
	s_nop 1
	s_nop 1
	s_nop 1
	s_nop 1
	s_nop 1
	s_nop 1
	s_nop 1
	s_nop 1
	s_nop 1
	s_nop 1
	s_nop 1
	s_waitcnt lgkmcnt(0)
	v_and_b32_e32 v252, 0x7f, v13
	v_cmp_gt_i32_e64 s[8:9], 0, v13
	v_xor_b32_e32 v13, 0x7f, v252
	s_nop 0
	v_cndmask_b32_e64 v7, v13, v252, s[8:9]
	v_lshl_add_u32 v7, v11, 7, v7
	v_bitop3_b32 v11, v6, s10, v6 bitop3:0xc
	v_cndmask_b32_e64 v6, v11, v10, s[6:7]
	v_lshrrev_b32_e32 v10, 4, v6
	v_lshl_add_u32 v252, v10, 8, v207
	ds_read_b32 v11, v252
	v_and_b32_e32 v6, 15, v6
	v_max_f32_e32 v13, v54, v55
	v_min_f32_e32 v55, v56, v58
	s_nop 0
	v_max_f32_e32 v58, v56, v58
	s_nop 0
	s_nop 1
	s_nop 1
	s_nop 1
	s_nop 1
	s_nop 1
	s_nop 1
	s_nop 1
	s_nop 1
	s_nop 1
	s_nop 1
	s_nop 1
	s_nop 1
	s_nop 1
	s_waitcnt lgkmcnt(0)
	v_and_b32_e32 v252, 0x7f, v11
	v_cmp_gt_i32_e64 s[6:7], 0, v11
	v_xor_b32_e32 v11, 0x7f, v252
	s_nop 0
	v_cndmask_b32_e64 v10, v11, v252, s[6:7]
	v_lshl_add_u32 v252, v6, 8, v207
	ds_read_b32 v11, v252 offset:4096
	s_nop 1
	s_nop 1
	s_nop 1
	s_nop 1
	s_nop 1
	s_nop 1
	s_nop 1
	s_nop 1
	s_nop 1
	s_nop 1
	s_nop 1
	s_nop 1
	s_nop 1
	s_nop 1
	s_nop 1
	s_nop 1
	s_waitcnt lgkmcnt(0)
	v_and_b32_e32 v252, 0x7f, v11
	v_cmp_gt_i32_e64 s[6:7], 0, v11
	v_xor_b32_e32 v11, 0x7f, v252
	s_nop 0
	v_cndmask_b32_e64 v6, v11, v252, s[6:7]
	v_lshl_add_u32 v6, v10, 7, v6
	v_min_f32_e32 v5, v4, v8
	v_and_b32_e32 v9, 0xff, v5
	v_bitop3_b32 v10, v5, s10, v5 bitop3:0xc
	v_cmp_gt_i32_e64 s[8:9], 0, v5
	v_and_b32_e32 v57, 0xffffff00, v5
	v_max_f32_e32 v4, v4, v8
	v_cndmask_b32_e64 v5, v10, v9, s[8:9]
	v_lshrrev_b32_e32 v9, 4, v5
	v_lshl_add_u32 v252, v9, 8, v207
	ds_read_b32 v10, v252
	v_and_b32_e32 v5, 15, v5
	v_and_b32_e32 v8, 0xff, v4
	v_cmp_gt_i32_e64 s[6:7], 0, v4
	v_and_b32_e32 v209, 0xffffff00, v4
	s_nop 1
	s_nop 1
	s_nop 1
	s_nop 1
	s_nop 1
	s_nop 1
	s_nop 1
	s_nop 1
	s_nop 1
	s_nop 1
	s_nop 1
	s_nop 1
	s_nop 1
	s_nop 1
	s_waitcnt lgkmcnt(0)
	v_and_b32_e32 v252, 0x7f, v10
	v_cmp_gt_i32_e64 s[8:9], 0, v10
	v_xor_b32_e32 v10, 0x7f, v252
	s_nop 0
	v_cndmask_b32_e64 v9, v10, v252, s[8:9]
	v_lshl_add_u32 v252, v5, 8, v207
	ds_read_b32 v10, v252 offset:4096
	s_nop 1
	s_nop 1
	s_nop 1
	s_nop 1
	s_nop 1
	s_nop 1
	s_nop 1
	s_nop 1
	s_nop 1
	s_nop 1
	s_nop 1
	s_nop 1
	s_nop 1
	s_nop 1
	s_nop 1
	s_nop 1
	s_waitcnt lgkmcnt(0)
	v_and_b32_e32 v252, 0x7f, v10
	v_cmp_gt_i32_e64 s[8:9], 0, v10
	v_xor_b32_e32 v10, 0x7f, v252
	s_nop 0
	v_cndmask_b32_e64 v5, v10, v252, s[8:9]
	v_lshl_add_u32 v5, v9, 7, v5
	v_bitop3_b32 v9, v4, s10, v4 bitop3:0xc
	v_cndmask_b32_e64 v4, v9, v8, s[6:7]
	v_lshrrev_b32_e32 v8, 4, v4
	v_lshl_add_u32 v252, v8, 8, v207
	ds_read_b32 v9, v252
	v_and_b32_e32 v4, 15, v4
	s_nop 0
	s_nop 1
	s_nop 1
	s_nop 1
	s_nop 1
	s_nop 1
	s_nop 1
	s_nop 1
	s_nop 1
	s_nop 1
	s_nop 1
	s_nop 1
	s_nop 1
	s_nop 1
	s_nop 1
	s_nop 1
	s_waitcnt lgkmcnt(0)
	v_and_b32_e32 v252, 0x7f, v9
	v_cmp_gt_i32_e64 s[6:7], 0, v9
	v_xor_b32_e32 v9, 0x7f, v252
	s_nop 0
	v_cndmask_b32_e64 v8, v9, v252, s[6:7]
	v_lshl_add_u32 v252, v4, 8, v207
	ds_read_b32 v9, v252 offset:4096
	s_nop 1
	s_nop 1
	s_nop 1
	s_nop 1
	s_nop 1
	s_nop 1
	s_nop 1
	s_nop 1
	s_nop 1
	s_nop 1
	s_nop 1
	s_nop 1
	s_nop 1
	s_nop 1
	s_nop 1
	s_nop 1
	s_waitcnt lgkmcnt(0)
	v_and_b32_e32 v252, 0x7f, v9
	v_cmp_gt_i32_e64 s[6:7], 0, v9
	v_xor_b32_e32 v9, 0x7f, v252
	s_nop 0
	v_cndmask_b32_e64 v4, v9, v252, s[6:7]
	v_lshl_add_u32 v4, v8, 7, v4
	v_min_f32_e32 v8, v13, v14
	v_min_f32_e32 v9, v15, v59
	v_max_f32_e32 v13, v13, v14
	v_max_f32_e32 v59, v15, v59
	v_min_f32_e32 v10, v8, v9
	v_max_f32_e32 v8, v8, v9
	v_min_f32_e32 v11, v10, v55
	v_and_b32_e32 v173, 0xff, v11
	v_bitop3_b32 v178, v11, s10, v11 bitop3:0xc
	v_cmp_gt_i32_e64 s[8:9], 0, v11
	v_and_b32_e32 v54, 0xffffff00, v11
	v_max_f32_e32 v10, v10, v55
	v_cndmask_b32_e64 v11, v178, v173, s[8:9]
	v_lshrrev_b32_e32 v173, 4, v11
	v_lshl_add_u32 v252, v173, 8, v207
	ds_read_b32 v178, v252
	v_and_b32_e32 v11, 15, v11
	v_cmp_gt_i32_e64 s[6:7], 0, v10
	v_and_b32_e32 v55, 0xffffff00, v10
	s_nop 0
	v_min_f32_e32 v14, v13, v59
	v_min_f32_e32 v62, v60, v61
	v_max_f32_e32 v59, v13, v59
	v_max_f32_e32 v60, v60, v61
	s_nop 0
	s_nop 0
	v_min_f32_e32 v13, v59, v60
	v_and_b32_e32 v61, 0xffffff00, v13
	v_max_f32_e32 v59, v59, v60
	v_cmp_gt_i32_e32 vcc, 0, v59
	v_and_b32_e32 v60, 0xffffff00, v59
	v_sub_f32_e32 v12, v12, v60
	v_mul_f32_e32 v12, 0x3fb8aa3b, v12
	s_nop 0
	s_nop 1
	s_nop 1
	s_nop 1
	s_nop 1
	s_nop 1
	s_nop 1
	s_nop 1
	s_waitcnt lgkmcnt(0)
	v_and_b32_e32 v252, 0x7f, v178
	v_cmp_gt_i32_e64 s[8:9], 0, v178
	v_xor_b32_e32 v178, 0x7f, v252
	s_nop 0
	v_cndmask_b32_e64 v173, v178, v252, s[8:9]
	v_lshl_add_u32 v252, v11, 8, v207
	ds_read_b32 v178, v252 offset:4096
	s_nop 1
	s_nop 1
	s_nop 1
	s_nop 1
	s_nop 1
	s_nop 1
	s_nop 1
	s_nop 1
	s_nop 1
	s_nop 1
	s_nop 1
	s_nop 1
	s_nop 1
	s_nop 1
	s_nop 1
	s_nop 1
	s_waitcnt lgkmcnt(0)
	v_and_b32_e32 v252, 0x7f, v178
	v_cmp_gt_i32_e64 s[8:9], 0, v178
	v_xor_b32_e32 v178, 0x7f, v252
	s_nop 0
	v_cndmask_b32_e64 v11, v178, v252, s[8:9]
	v_lshl_add_u32 v11, v173, 7, v11
	v_and_b32_e32 v173, 0xff, v10
	v_bitop3_b32 v178, v10, s10, v10 bitop3:0xc
	v_cndmask_b32_e64 v10, v178, v173, s[6:7]
	v_lshrrev_b32_e32 v173, 4, v10
	v_lshl_add_u32 v252, v173, 8, v207
	ds_read_b32 v178, v252
	v_and_b32_e32 v10, 15, v10
	s_nop 0
	s_nop 1
	s_nop 1
	s_nop 1
	s_nop 1
	s_nop 1
	s_nop 1
	s_nop 1
	s_nop 1
	s_nop 1
	s_nop 1
	s_nop 1
	s_nop 1
	s_nop 1
	s_nop 1
	s_nop 1
	s_waitcnt lgkmcnt(0)
	v_and_b32_e32 v252, 0x7f, v178
	v_cmp_gt_i32_e64 s[6:7], 0, v178
	v_xor_b32_e32 v178, 0x7f, v252
	s_nop 0
	v_cndmask_b32_e64 v173, v178, v252, s[6:7]
	v_lshl_add_u32 v252, v10, 8, v207
	ds_read_b32 v178, v252 offset:4096
	s_nop 1
	s_nop 1
	s_nop 1
	s_nop 1
	s_nop 1
	s_nop 1
	s_nop 1
	s_nop 1
	s_nop 1
	s_nop 1
	s_nop 1
	s_nop 1
	s_nop 1
	s_nop 1
	s_nop 1
	s_nop 1
	s_waitcnt lgkmcnt(0)
	v_and_b32_e32 v252, 0x7f, v178
	v_cmp_gt_i32_e64 s[6:7], 0, v178
	v_xor_b32_e32 v178, 0x7f, v252
	s_nop 0
	v_cndmask_b32_e64 v10, v178, v252, s[6:7]
	v_lshl_add_u32 v10, v173, 7, v10
	v_min_f32_e32 v9, v8, v58
	v_and_b32_e32 v173, 0xff, v9
	v_bitop3_b32 v178, v9, s10, v9 bitop3:0xc
	v_cmp_gt_i32_e64 s[8:9], 0, v9
	v_and_b32_e32 v56, 0xffffff00, v9
	v_max_f32_e32 v8, v8, v58
	v_cndmask_b32_e64 v9, v178, v173, s[8:9]
	v_lshrrev_b32_e32 v173, 4, v9
	v_lshl_add_u32 v252, v173, 8, v207
	ds_read_b32 v178, v252
	v_and_b32_e32 v9, 15, v9
	v_cmp_gt_i32_e64 s[6:7], 0, v8
	v_and_b32_e32 v58, 0xffffff00, v8
	s_nop 0
	s_nop 1
	s_nop 1
	s_nop 1
	s_nop 1
	s_nop 1
	s_nop 1
	s_nop 1
	s_nop 1
	s_nop 1
	s_nop 1
	s_nop 1
	s_nop 1
	s_nop 1
	s_nop 1
	s_waitcnt lgkmcnt(0)
	v_and_b32_e32 v252, 0x7f, v178
	v_cmp_gt_i32_e64 s[8:9], 0, v178
	v_xor_b32_e32 v178, 0x7f, v252
	s_nop 0
	v_cndmask_b32_e64 v173, v178, v252, s[8:9]
	v_lshl_add_u32 v252, v9, 8, v207
	ds_read_b32 v178, v252 offset:4096
	s_nop 1
	s_nop 1
	s_nop 1
	s_nop 1
	s_nop 1
	s_nop 1
	s_nop 1
	s_nop 1
	s_nop 1
	s_nop 1
	s_nop 1
	s_nop 1
	s_nop 1
	s_nop 1
	s_nop 1
	s_nop 1
	s_waitcnt lgkmcnt(0)
	v_and_b32_e32 v252, 0x7f, v178
	v_cmp_gt_i32_e64 s[8:9], 0, v178
	v_xor_b32_e32 v178, 0x7f, v252
	s_nop 0
	v_cndmask_b32_e64 v9, v178, v252, s[8:9]
	v_lshl_add_u32 v9, v173, 7, v9
	v_and_b32_e32 v173, 0xff, v8
	v_bitop3_b32 v178, v8, s10, v8 bitop3:0xc
	v_cndmask_b32_e64 v8, v178, v173, s[6:7]
	v_lshrrev_b32_e32 v173, 4, v8
	v_lshl_add_u32 v252, v173, 8, v207
	ds_read_b32 v178, v252
	v_and_b32_e32 v8, 15, v8
	s_nop 0
	s_nop 1
	s_nop 1
	s_nop 1
	s_nop 1
	s_nop 1
	s_nop 1
	s_nop 1
	s_nop 1
	s_nop 1
	s_nop 1
	s_nop 1
	s_nop 1
	s_nop 1
	s_nop 1
	s_nop 1
	s_waitcnt lgkmcnt(0)
	v_and_b32_e32 v252, 0x7f, v178
	v_cmp_gt_i32_e64 s[6:7], 0, v178
	v_xor_b32_e32 v178, 0x7f, v252
	s_nop 0
	v_cndmask_b32_e64 v173, v178, v252, s[6:7]
	v_lshl_add_u32 v252, v8, 8, v207
	ds_read_b32 v178, v252 offset:4096
	s_nop 1
	s_nop 1
	s_nop 1
	s_nop 1
	s_nop 1
	s_nop 1
	s_nop 1
	s_nop 1
	s_nop 1
	s_nop 1
	s_nop 1
	s_nop 1
	s_nop 1
	s_nop 1
	s_nop 1
	s_nop 1
	s_waitcnt lgkmcnt(0)
	v_and_b32_e32 v252, 0x7f, v178
	v_cmp_gt_i32_e64 s[6:7], 0, v178
	v_xor_b32_e32 v178, 0x7f, v252
	s_nop 0
	v_cndmask_b32_e64 v8, v178, v252, s[6:7]
	v_lshl_add_u32 v8, v173, 7, v8
	v_min_f32_e32 v15, v14, v62
	v_and_b32_e32 v173, 0xff, v15
	v_bitop3_b32 v178, v15, s10, v15 bitop3:0xc
	v_cmp_gt_i32_e64 s[8:9], 0, v15
	v_and_b32_e32 v63, 0xffffff00, v15
	v_max_f32_e32 v14, v14, v62
	v_cndmask_b32_e64 v15, v178, v173, s[8:9]
	v_lshrrev_b32_e32 v173, 4, v15
	v_lshl_add_u32 v252, v173, 8, v207
	ds_read_b32 v178, v252
	v_and_b32_e32 v15, 15, v15
	v_cmp_gt_i32_e64 s[6:7], 0, v14
	v_and_b32_e32 v62, 0xffffff00, v14
	s_nop 0
	s_nop 1
	s_nop 1
	s_nop 1
	s_nop 1
	s_nop 1
	s_nop 1
	s_nop 1
	s_nop 1
	s_nop 1
	s_nop 1
	s_nop 1
	s_nop 1
	s_nop 1
	s_nop 1
	s_waitcnt lgkmcnt(0)
	v_and_b32_e32 v252, 0x7f, v178
	v_cmp_gt_i32_e64 s[8:9], 0, v178
	v_xor_b32_e32 v178, 0x7f, v252
	s_nop 0
	v_cndmask_b32_e64 v173, v178, v252, s[8:9]
	v_lshl_add_u32 v252, v15, 8, v207
	ds_read_b32 v178, v252 offset:4096
	s_nop 1
	s_nop 1
	s_nop 1
	s_nop 1
	s_nop 1
	s_nop 1
	s_nop 1
	s_nop 1
	s_nop 1
	s_nop 1
	s_nop 1
	s_nop 1
	s_nop 1
	s_nop 1
	s_nop 1
	s_nop 1
	s_waitcnt lgkmcnt(0)
	v_and_b32_e32 v252, 0x7f, v178
	v_cmp_gt_i32_e64 s[8:9], 0, v178
	v_xor_b32_e32 v178, 0x7f, v252
	s_nop 0
	v_cndmask_b32_e64 v15, v178, v252, s[8:9]
	v_lshl_add_u32 v15, v173, 7, v15
	v_and_b32_e32 v173, 0xff, v14
	v_bitop3_b32 v178, v14, s10, v14 bitop3:0xc
	v_cndmask_b32_e64 v14, v178, v173, s[6:7]
	v_lshrrev_b32_e32 v173, 4, v14
	v_lshl_add_u32 v252, v173, 8, v207
	ds_read_b32 v178, v252
	v_and_b32_e32 v14, 15, v14
	v_readlane_b32 s8, v253, 23
	v_readlane_b32 s9, v253, 24
	s_nop 0
	s_nop 1
	s_nop 1
	s_nop 1
	s_nop 1
	s_nop 1
	s_nop 1
	s_nop 1
	s_nop 1
	s_nop 1
	s_nop 1
	s_nop 1
	s_nop 1
	s_nop 1
	s_nop 1
	s_waitcnt lgkmcnt(0)
	v_and_b32_e32 v252, 0x7f, v178
	v_cmp_gt_i32_e64 s[6:7], 0, v178
	v_xor_b32_e32 v178, 0x7f, v252
	s_nop 0
	v_cndmask_b32_e64 v173, v178, v252, s[6:7]
	v_lshl_add_u32 v252, v14, 8, v207
	ds_read_b32 v178, v252 offset:4096
	s_nop 1
	s_nop 1
	s_nop 1
	s_nop 1
	s_nop 1
	s_nop 1
	s_nop 1
	s_nop 1
	s_nop 1
	s_nop 1
	s_nop 1
	s_nop 1
	s_nop 1
	s_nop 1
	s_nop 1
	s_nop 1
	s_waitcnt lgkmcnt(0)
	v_and_b32_e32 v252, 0x7f, v178
	v_cmp_gt_i32_e64 s[6:7], 0, v178
	v_xor_b32_e32 v178, 0x7f, v252
	s_nop 0
	v_cndmask_b32_e64 v14, v178, v252, s[6:7]
	v_lshl_add_u32 v14, v173, 7, v14
	v_and_b32_e32 v173, 0xff, v13
	v_bitop3_b32 v178, v13, s10, v13 bitop3:0xc
	v_cmp_gt_i32_e64 s[6:7], 0, v13
	s_nop 1
	v_cndmask_b32_e64 v13, v178, v173, s[6:7]
	v_lshrrev_b32_e32 v173, 4, v13
	v_lshl_add_u32 v252, v173, 8, v207
	ds_read_b32 v178, v252
	v_and_b32_e32 v13, 15, v13
	s_nop 0
	s_nop 1
	s_nop 1
	s_nop 1
	s_nop 1
	s_nop 1
	s_nop 1
	s_nop 1
	s_nop 1
	s_nop 1
	s_nop 1
	s_nop 1
	s_nop 1
	s_nop 1
	s_nop 1
	s_nop 1
	s_waitcnt lgkmcnt(0)
	v_and_b32_e32 v252, 0x7f, v178
	v_cmp_gt_i32_e64 s[6:7], 0, v178
	v_xor_b32_e32 v178, 0x7f, v252
	s_nop 0
	v_cndmask_b32_e64 v173, v178, v252, s[6:7]
	v_lshl_add_u32 v252, v13, 8, v207
	ds_read_b32 v178, v252 offset:4096
	s_nop 1
	s_nop 1
	s_nop 1
	s_nop 1
	s_nop 1
	s_nop 1
	s_nop 1
	s_nop 1
	s_nop 1
	s_nop 1
	s_nop 1
	s_nop 1
	s_nop 1
	s_nop 1
	s_nop 1
	s_nop 1
	s_waitcnt lgkmcnt(0)
	v_and_b32_e32 v252, 0x7f, v178
	v_cmp_gt_i32_e64 s[6:7], 0, v178
	v_xor_b32_e32 v178, 0x7f, v252
	s_nop 0
	v_cndmask_b32_e64 v13, v178, v252, s[6:7]
	v_lshl_add_u32 v13, v173, 7, v13
	v_and_b32_e32 v173, 0xff, v59
	v_bitop3_b32 v178, v59, s10, v59 bitop3:0xc
	v_cndmask_b32_e32 v59, v178, v173, vcc
	v_lshrrev_b32_e32 v173, 4, v59
	v_cmp_gt_u32_e32 vcc, 16, v59
	s_nop 1
	v_cndmask_b32_e32 v49, 0, v49, vcc
	v_cmp_eq_u32_e32 vcc, 1, v173
	s_nop 1
	v_cndmask_b32_e32 v48, v49, v48, vcc
	v_cmp_eq_u32_e32 vcc, 2, v173
	s_nop 1
	v_cndmask_b32_e32 v47, v48, v47, vcc
	v_cmp_eq_u32_e32 vcc, 3, v173
	s_nop 1
	v_cndmask_b32_e32 v46, v47, v46, vcc
	v_cmp_eq_u32_e32 vcc, 4, v173
	s_nop 1
	v_cndmask_b32_e32 v45, v46, v45, vcc
	v_cmp_eq_u32_e32 vcc, 5, v173
	s_nop 1
	v_cndmask_b32_e32 v44, v45, v44, vcc
	v_cmp_eq_u32_e32 vcc, 6, v173
	s_nop 1
	v_cndmask_b32_e32 v43, v44, v43, vcc
	v_cmp_eq_u32_e32 vcc, 7, v173
	s_nop 1
	v_cndmask_b32_e32 v42, v43, v42, vcc
	v_cmp_eq_u32_e32 vcc, 8, v173
	s_nop 1
	v_cndmask_b32_e32 v41, v42, v41, vcc
	v_cmp_eq_u32_e32 vcc, 9, v173
	s_nop 1
	v_cndmask_b32_e32 v40, v41, v40, vcc
	v_cmp_eq_u32_e32 vcc, 10, v173
	s_nop 1
	v_cndmask_b32_e32 v39, v40, v39, vcc
	v_cmp_eq_u32_e32 vcc, 11, v173
	s_nop 1
	v_cndmask_b32_e32 v38, v39, v38, vcc
	v_cmp_eq_u32_e32 vcc, 12, v173
	v_and_b32_e32 v39, 15, v59
	s_nop 0
	v_cndmask_b32_e32 v37, v38, v37, vcc
	v_cmp_eq_u32_e32 vcc, 13, v173
	s_nop 1
	v_cndmask_b32_e32 v36, v37, v36, vcc
	v_cmp_eq_u32_e32 vcc, 14, v173
	s_nop 1
	v_cndmask_b32_e32 v35, v36, v35, vcc
	v_cmp_eq_u32_e32 vcc, 15, v173
	v_exp_f32_e32 v36, v12
	v_and_b32_e32 v12, 0xffffff00, v32
	v_cndmask_b32_e32 v38, v35, v34, vcc
	v_cmp_eq_u32_e32 vcc, 0, v39
	v_sub_f32_e32 v12, v12, v60
	v_mul_f32_e32 v12, 0x3fb8aa3b, v12
	v_cndmask_b32_e32 v33, 0, v33, vcc
	v_cmp_eq_u32_e32 vcc, 1, v39
	v_exp_f32_e32 v37, v12
	s_nop 0
	v_cndmask_b32_e32 v17, v33, v17, vcc
	v_cmp_eq_u32_e32 vcc, 2, v39
	v_sub_f32_e32 v33, v51, v60
	v_mul_f32_e32 v33, 0x3fb8aa3b, v33
	v_cndmask_b32_e32 v17, v17, v18, vcc
	v_cmp_eq_u32_e32 vcc, 3, v39
	v_sub_f32_e32 v18, v60, v60
	v_mul_f32_e32 v18, 0x3fb8aa3b, v18
	v_cndmask_b32_e32 v17, v17, v19, vcc
	v_cmp_eq_u32_e32 vcc, 4, v39
	v_sub_f32_e32 v19, v61, v60
	v_exp_f32_e32 v18, v18
	v_cndmask_b32_e32 v17, v17, v20, vcc
	v_cmp_eq_u32_e32 vcc, 5, v39
	v_mul_f32_e32 v19, 0x3fb8aa3b, v19
	v_sub_f32_e32 v20, v62, v60
	v_cndmask_b32_e32 v17, v17, v21, vcc
	v_exp_f32_e32 v19, v19
	v_mul_f32_e32 v20, 0x3fb8aa3b, v20
	v_sub_f32_e32 v21, v63, v60
	v_cmp_eq_u32_e32 vcc, 6, v39
	v_exp_f32_e32 v20, v20
	v_mul_f32_e32 v21, 0x3fb8aa3b, v21
	v_cndmask_b32_e32 v17, v17, v22, vcc
	v_cmp_eq_u32_e32 vcc, 7, v39
	v_exp_f32_e32 v21, v21
	v_add_f32_e32 v22, 0, v18
	v_cndmask_b32_e32 v17, v17, v23, vcc
	v_cmp_eq_u32_e32 vcc, 8, v39
	v_add_f32_e32 v22, v19, v22
	v_add_f32_e32 v22, v20, v22
	v_cndmask_b32_e32 v17, v17, v24, vcc
	v_cmp_eq_u32_e32 vcc, 9, v39
	v_sub_f32_e32 v23, v56, v60
	v_mul_f32_e32 v23, 0x3fb8aa3b, v23
	v_cndmask_b32_e32 v17, v17, v25, vcc
	v_cmp_eq_u32_e32 vcc, 10, v39
	v_sub_f32_e32 v24, v55, v60
	v_exp_f32_e32 v23, v23
	v_cndmask_b32_e32 v17, v17, v26, vcc
	v_add_f32_e32 v26, v21, v22
	v_sub_f32_e32 v22, v58, v60
	v_mul_f32_e32 v22, 0x3fb8aa3b, v22
	v_exp_f32_e32 v22, v22
	v_mul_f32_e32 v24, 0x3fb8aa3b, v24
	v_sub_f32_e32 v25, v54, v60
	v_exp_f32_e32 v24, v24
	v_mul_f32_e32 v25, 0x3fb8aa3b, v25
	v_cmp_eq_u32_e32 vcc, 11, v39
	v_exp_f32_e32 v25, v25
	v_add_f32_e32 v26, v22, v26
	v_cndmask_b32_e32 v17, v17, v27, vcc
	v_cmp_eq_u32_e32 vcc, 12, v39
	v_add_f32_e32 v26, v23, v26
	v_add_f32_e32 v26, v24, v26
	v_cndmask_b32_e32 v17, v17, v28, vcc
	v_cmp_eq_u32_e32 vcc, 13, v39
	v_sub_f32_e32 v27, v57, v60
	v_mul_f32_e32 v27, 0x3fb8aa3b, v27
	v_cndmask_b32_e32 v17, v17, v29, vcc
	v_cmp_eq_u32_e32 vcc, 14, v39
	v_sub_f32_e32 v28, v53, v60
	v_exp_f32_e32 v27, v27
	v_cndmask_b32_e32 v17, v17, v30, vcc
	v_add_f32_e32 v30, v25, v26
	v_sub_f32_e32 v26, v209, v60
	v_mul_f32_e32 v26, 0x3fb8aa3b, v26
	v_exp_f32_e32 v26, v26
	v_mul_f32_e32 v28, 0x3fb8aa3b, v28
	v_sub_f32_e32 v29, v52, v60
	v_exp_f32_e32 v28, v28
	v_mul_f32_e32 v29, 0x3fb8aa3b, v29
	v_exp_f32_e32 v29, v29
	v_exp_f32_e32 v34, v33
	v_sub_f32_e32 v33, v50, v60
	v_add_f32_e32 v30, v26, v30
	v_mul_f32_e32 v33, 0x3fb8aa3b, v33
	v_add_f32_e32 v30, v27, v30
	v_exp_f32_e32 v35, v33
	v_add_f32_e32 v30, v28, v30
	v_add_f32_e32 v30, v29, v30
	v_add_f32_e32 v12, v34, v30
	v_add_f32_e32 v12, v35, v12
	v_add_f32_e32 v12, v36, v12
	v_add_f32_e32 v30, v37, v12
	v_div_scale_f32 v32, s[6:7], v30, v30, 1.0
	v_rcp_f32_e32 v33, v32
	v_cmp_eq_u32_e32 vcc, 15, v39
	v_readlane_b32 s6, v255, 46
	s_lshl_b32 s6, s6, 4
	v_cndmask_b32_e32 v12, v17, v31, vcc
	v_fma_f32 v17, -v32, v33, 1.0
	v_fmac_f32_e32 v33, v17, v33
	v_div_scale_f32 v17, vcc, 1.0, v30, 1.0
	v_mul_f32_e32 v31, v17, v33
	v_lshl_add_u32 v12, v38, 7, v12
	v_fma_f32 v38, -v32, v31, v17
	v_fmac_f32_e32 v31, v38, v33
	v_fma_f32 v17, -v32, v31, v17
	v_div_fmas_f32 v17, v17, v33, v31
	v_div_fixup_f32 v30, v17, v30, 1.0
	v_lshlrev_b64 v[16:17], 9, v[176:177]
	s_ashr_i32 s7, s6, 31
	v_lshl_add_u64 v[32:33], s[94:95], 0, v[16:17]
	s_lshl_b64 s[6:7], s[6:7], 2
	v_lshl_add_u64 v[32:33], v[32:33], 0, s[6:7]
	v_lshl_add_u64 v[16:17], s[8:9], 0, v[16:17]
	v_lshl_add_u64 v[16:17], v[16:17], 0, s[6:7]
	global_store_dwordx4 v[32:33], v[12:15], off
	v_readlane_b32 s8, v255, 44
	v_readlane_b32 s9, v255, 45
	v_pk_mul_f32 v[12:13], v[18:19], v[30:31] op_sel_hi:[1,0]
	v_pk_mul_f32 v[14:15], v[20:21], v[30:31] op_sel_hi:[1,0]
	global_store_dwordx4 v[16:17], v[12:15], off
	global_store_dwordx4 v[32:33], v[8:11], off offset:16
	s_nop 1
	v_pk_mul_f32 v[8:9], v[22:23], v[30:31] op_sel_hi:[1,0]
	v_pk_mul_f32 v[10:11], v[24:25], v[30:31] op_sel_hi:[1,0]
	global_store_dwordx4 v[16:17], v[8:11], off offset:16
	global_store_dwordx4 v[32:33], v[4:7], off offset:32
	s_nop 1
	v_pk_mul_f32 v[4:5], v[26:27], v[30:31] op_sel_hi:[1,0]
	v_pk_mul_f32 v[6:7], v[28:29], v[30:31] op_sel_hi:[1,0]
	global_store_dwordx4 v[16:17], v[4:7], off offset:32
	global_store_dwordx4 v[32:33], v[0:3], off offset:48
	s_nop 1
	v_pk_mul_f32 v[0:1], v[34:35], v[30:31] op_sel_hi:[1,0]
	v_pk_mul_f32 v[2:3], v[36:37], v[30:31] op_sel_hi:[1,0]
	global_store_dwordx4 v[16:17], v[0:3], off offset:48
	s_branch .LBB0_696
